# scanner software-pipelined across chunks (loader one more chunk ahead, next-chunk LDS reads issued before the barrier, y reduce-scatter tail finished inside the next chunk), 4 rotating input register
# baseline (speedup 1.0000x reference)
.LBB0_604:
	s_ashr_i32 s1, s57, 2
	s_and_b32 s0, s57, 7
	s_and_b32 s1, s1, -8
	s_or_b32 s0, s1, s0
	s_ashr_i32 s1, s0, 1
	s_lshr_b32 s6, s1, 30
	s_add_i32 s6, s1, s6
	s_and_b32 s6, s6, -4
	s_waitcnt lgkmcnt(0)
	s_sub_i32 s51, s1, s6
	s_ashr_i32 s1, s57, 31
	s_lshr_b32 s1, s1, 29
	s_add_i32 s0, s0, s1
	s_bfe_u32 s7, s57, 0x20003
	s_and_b32 s50, s57, 1
	s_ashr_i32 s6, s0, 3
	s_mov_b64 s[0:1], -1
	s_and_b64 vcc, exec, s[64:65]
	s_barrier
	s_cbranch_vccz .LBB0_617
	s_load_dwordx2 s[0:1], s[58:59], 0x1e8
	s_mul_i32 s8, s50, 0x1100000
	v_mov_b32_e32 v14, 0
	v_bfrev_b32_e32 v89, v85
	v_and_b32_e32 v112, 2, v85
	v_and_b32_e32 v113, 1, v85
	v_lshrrev_b32_e32 v89, 28, v89
	v_cmp_ne_u32_e64 s[14:15], 0, v112
	v_cmp_ne_u32_e64 s[16:17], 0, v113
	v_or_b32_e32 v94, 16, v89
	v_mov_b32_e32 v15, v14
	v_mov_b32_e32 v16, v14
	s_waitcnt lgkmcnt(0)
	s_add_u32 s8, s0, s8
	s_addc_u32 s9, s1, 0
	s_lshl_b32 s0, s51, 6
	s_ashr_i32 s1, s0, 31
	s_lshl_b64 s[0:1], s[0:1], 1
	s_add_u32 s0, s8, s0
	s_addc_u32 s1, s9, s1
	s_lshl_b32 s8, s7, 5
	s_add_u32 s0, s0, s8
	s_addc_u32 s1, s1, 0
	s_cmp_lg_u32 s50, 0
	v_lshl_add_u64 v[10:11], v[82:83], 1, s[0:1]
	s_cselect_b64 s[0:1], -1, 0
	s_lshl_b32 s70, s6, 12
	s_lshl_b32 s33, s6, 8
	s_mov_b32 s8, 0
	s_add_i32 s9, s70, 0x10ff
	s_add_i32 s52, s33, 0x80ff
	s_addk_i32 s70, 0xff00
	s_add_i32 s71, s33, 0x8000
	v_mov_b32_e32 v17, v14
	s_barrier
	v_mov_b32_e32 v18, v87
	v_add_u32_e32 v2, 0xa000, v96
	ds_read_b128 v[20:23], v18
	ds_read_b128 v[28:31], v18 offset:24576
	ds_read2_b32 v[120:121], v2 offset1:16
	ds_read_b128 v[24:27], v18 offset:8192
	ds_read_b128 v[32:35], v18 offset:32768
	ds_read_b128 v[36:39], v18 offset:256
	ds_read_b128 v[44:47], v18 offset:24832
	ds_read_b128 v[40:43], v18 offset:8448
	ds_read_b128 v[48:51], v18 offset:33024
	s_branch .LBB0_608

.LBB0_607:
	s_mul_i32 s33, s8, 0xab
	s_bfe_u32 s33, s33, 0x70009
	s_mul_i32 s33, s33, 3
	s_sub_i32 s33, s8, s33
	s_and_b32 s33, s33, 0xff
	s_mul_i32 s33, s33, 0xa800
	s_add_i32 s33, s33, 0
	s_waitcnt vmcnt(0)
	s_add_i32 s18, s33, 0xa800
	s_cmp_eq_u32 s18, 0x1f800
	s_cselect_b32 s18, 0, s18
	s_ashr_i32 s47, s46, 31
	s_lshl_b64 s[46:47], s[46:47], 9
	v_add_u32_e32 v18, s33, v87
	v_add_u32_e32 v19, s33, v96
	v_add_u32_e32 v68, s18, v87
	v_add_u32_e32 v69, s18, v96
	v_add_u32_e32 v2, 0xa000, v19
	v_add_u32_e32 v3, 0xa400, v19
	v_add_u32_e32 v69, 0xa000, v69
	s_waitcnt lgkmcnt(5)
	v_pk_mul_f32 v[126:127], v[14:15], v[20:21]
	v_pk_mul_f32 v[128:129], v[14:15], v[112:113]
	v_pk_fma_f32 v[126:127], v[16:17], v[22:23], v[126:127]
	v_pk_fma_f32 v[128:129], v[16:17], v[114:115], v[128:129]
	v_add_f32_e32 v124, v126, v127
	v_pk_fma_f32 v[14:15], v[28:29], v[120:121], v[14:15] op_sel_hi:[1,0,1]
	v_add_f32_e32 v131, v128, v129
	v_add_f32_dpp v124, v124, v124 quad_perm:[1,0,3,2] row_mask:0xf bank_mask:0xf bound_ctrl:1
	v_pk_fma_f32 v[16:17], v[30:31], v[120:121], v[16:17] op_sel_hi:[1,0,1]
	ds_read_b128 v[52:55], v18 offset:512
	v_add_f32_dpp v124, v124, v124 quad_perm:[2,3,0,1] row_mask:0xf bank_mask:0xf bound_ctrl:1
	ds_read_b128 v[60:63], v18 offset:25088
	ds_read2_b32 v[122:123], v2 offset0:32 offset1:48
	v_add_f32_dpp v124, v124, v124 row_half_mirror row_mask:0xf bank_mask:0xf bound_ctrl:1
	ds_read_b128 v[56:59], v18 offset:8704
	ds_read_b128 v[64:67], v18 offset:33280
	v_add_f32_dpp v124, v124, v124 row_mirror row_mask:0xf bank_mask:0xf bound_ctrl:1
	v_pk_fma_f32 v[14:15], v[24:25], v[124:125], v[14:15] op_sel_hi:[1,0,1] neg_lo:[0,1,0] neg_hi:[0,1,0]
	v_pk_fma_f32 v[16:17], v[26:27], v[124:125], v[16:17] op_sel_hi:[1,0,1] neg_lo:[0,1,0] neg_hi:[0,1,0]
	v_add_f32_dpp v133, v130, v130 row_mirror row_mask:0xf bank_mask:0x3 bound_ctrl:1
	s_waitcnt lgkmcnt(6)
	v_pk_mul_f32 v[126:127], v[14:15], v[36:37]
	v_pk_mul_f32 v[128:129], v[14:15], v[32:33]
	v_pk_fma_f32 v[126:127], v[16:17], v[38:39], v[126:127]
	v_pk_fma_f32 v[128:129], v[16:17], v[34:35], v[128:129]
	v_add_f32_e32 v124, v126, v127
	v_pk_fma_f32 v[14:15], v[44:45], v[120:121], v[14:15] op_sel:[0,1,0]
	v_add_f32_e32 v130, v128, v129
	v_add_f32_dpp v124, v124, v124 quad_perm:[1,0,3,2] row_mask:0xf bank_mask:0xf bound_ctrl:1
	v_pk_fma_f32 v[16:17], v[46:47], v[120:121], v[16:17] op_sel:[0,1,0]
	ds_read_b128 v[100:103], v18 offset:768
	v_add_f32_dpp v124, v124, v124 quad_perm:[2,3,0,1] row_mask:0xf bank_mask:0xf bound_ctrl:1
	ds_read_b128 v[108:111], v18 offset:25344
	ds_read_b128 v[116:119], v18 offset:17152
	v_add_f32_dpp v124, v124, v124 row_half_mirror row_mask:0xf bank_mask:0xf bound_ctrl:1
	ds_read_b128 v[104:107], v18 offset:8960
	ds_read_b128 v[112:115], v18 offset:33536
	v_add_f32_dpp v124, v124, v124 row_mirror row_mask:0xf bank_mask:0xf bound_ctrl:1
	v_pk_fma_f32 v[14:15], v[40:41], v[124:125], v[14:15] op_sel_hi:[1,0,1] neg_lo:[0,1,0] neg_hi:[0,1,0]
	v_pk_fma_f32 v[16:17], v[42:43], v[124:125], v[16:17] op_sel_hi:[1,0,1] neg_lo:[0,1,0] neg_hi:[0,1,0]
	v_add_f32_dpp v133, v131, v131 row_mirror row_mask:0xf bank_mask:0xc bound_ctrl:1
	v_add_f32_dpp v135, v132, v132 row_half_mirror row_mask:0xf bank_mask:0x5 bound_ctrl:1
	s_waitcnt lgkmcnt(6)
	v_pk_mul_f32 v[126:127], v[14:15], v[52:53]
	v_pk_mul_f32 v[128:129], v[14:15], v[48:49]
	v_pk_fma_f32 v[126:127], v[16:17], v[54:55], v[126:127]
	v_pk_fma_f32 v[128:129], v[16:17], v[50:51], v[128:129]
	v_add_f32_e32 v124, v126, v127
	v_pk_fma_f32 v[14:15], v[60:61], v[122:123], v[14:15] op_sel_hi:[1,0,1]
	v_add_f32_e32 v131, v128, v129
	v_add_f32_dpp v124, v124, v124 quad_perm:[1,0,3,2] row_mask:0xf bank_mask:0xf bound_ctrl:1
	v_pk_fma_f32 v[16:17], v[62:63], v[122:123], v[16:17] op_sel_hi:[1,0,1]
	ds_read_b128 v[20:23], v18 offset:1024
	v_add_f32_dpp v124, v124, v124 quad_perm:[2,3,0,1] row_mask:0xf bank_mask:0xf bound_ctrl:1
	ds_read_b128 v[28:31], v18 offset:25600
	ds_read2_b32 v[120:121], v2 offset0:64 offset1:80
	v_add_f32_dpp v124, v124, v124 row_half_mirror row_mask:0xf bank_mask:0xf bound_ctrl:1
	ds_read_b128 v[24:27], v18 offset:9216
	ds_read_b128 v[32:35], v18 offset:33792
	v_add_f32_dpp v124, v124, v124 row_mirror row_mask:0xf bank_mask:0xf bound_ctrl:1
	v_pk_fma_f32 v[14:15], v[56:57], v[124:125], v[14:15] op_sel_hi:[1,0,1] neg_lo:[0,1,0] neg_hi:[0,1,0]
	v_pk_fma_f32 v[16:17], v[58:59], v[124:125], v[16:17] op_sel_hi:[1,0,1] neg_lo:[0,1,0] neg_hi:[0,1,0]
	v_lshl_add_u64 v[12:13], v[10:11], 0, s[46:47]
	v_mul_hi_i32_i24_e32 v5, s44, v89
	v_mul_i32_i24_e32 v4, s44, v89
	v_add_f32_dpp v135, v133, v133 row_half_mirror row_mask:0xf bank_mask:0xa bound_ctrl:1
	v_add_f32_dpp v138, v134, v134 quad_perm:[2,3,0,1] row_mask:0xf bank_mask:0xf bound_ctrl:1
	s_nop 0
	v_add_f32_dpp v98, v135, v135 quad_perm:[2,3,0,1] row_mask:0xf bank_mask:0xf bound_ctrl:1
	v_cndmask_b32_e64 v137, v138, v98, s[14:15]
	v_add_f32_dpp v138, v136, v136 quad_perm:[1,0,3,2] row_mask:0xf bank_mask:0xf bound_ctrl:1
	s_nop 0
	v_add_f32_dpp v98, v137, v137 quad_perm:[1,0,3,2] row_mask:0xf bank_mask:0xf bound_ctrl:1
	v_cndmask_b32_e64 v99, v138, v98, s[16:17]
	v_bfe_u32 v7, v99, 16, 1
	v_add3_u32 v7, v99, v7, s3
	s_cmp_eq_u32 s8, 0
	s_cbranch_scc1 .Lsc_nost
	global_store_short_d16_hi v[8:9], v7, off
.Lsc_nost:
	v_add_f32_dpp v132, v130, v130 row_mirror row_mask:0xf bank_mask:0x3 bound_ctrl:1
	s_waitcnt lgkmcnt(6)
	v_pk_mul_f32 v[126:127], v[14:15], v[100:101]
	v_pk_mul_f32 v[128:129], v[14:15], v[64:65]
	v_pk_fma_f32 v[126:127], v[16:17], v[102:103], v[126:127]
	v_pk_fma_f32 v[128:129], v[16:17], v[66:67], v[128:129]
	v_add_f32_e32 v124, v126, v127
	v_pk_fma_f32 v[14:15], v[108:109], v[122:123], v[14:15] op_sel:[0,1,0]
	v_add_f32_e32 v130, v128, v129
	v_add_f32_dpp v124, v124, v124 quad_perm:[1,0,3,2] row_mask:0xf bank_mask:0xf bound_ctrl:1
	v_pk_fma_f32 v[16:17], v[110:111], v[122:123], v[16:17] op_sel:[0,1,0]
	ds_read_b128 v[36:39], v18 offset:1280
	v_add_f32_dpp v124, v124, v124 quad_perm:[2,3,0,1] row_mask:0xf bank_mask:0xf bound_ctrl:1
	ds_read_b128 v[44:47], v18 offset:25856
	ds_read_b128 v[40:43], v18 offset:9472
	v_add_f32_dpp v124, v124, v124 row_half_mirror row_mask:0xf bank_mask:0xf bound_ctrl:1
	ds_read_b128 v[48:51], v18 offset:34048
	v_lshl_add_u64 v[4:5], v[4:5], 1, v[12:13]
	v_add_f32_dpp v124, v124, v124 row_mirror row_mask:0xf bank_mask:0xf bound_ctrl:1
	v_pk_fma_f32 v[14:15], v[104:105], v[124:125], v[14:15] op_sel_hi:[1,0,1] neg_lo:[0,1,0] neg_hi:[0,1,0]
	v_pk_fma_f32 v[16:17], v[106:107], v[124:125], v[16:17] op_sel_hi:[1,0,1] neg_lo:[0,1,0] neg_hi:[0,1,0]
	v_pk_mul_f32 v[14:15], v[14:15], v[116:117]
	v_pk_mul_f32 v[16:17], v[16:17], v[118:119]
	v_add_f32_dpp v132, v131, v131 row_mirror row_mask:0xf bank_mask:0xc bound_ctrl:1
	s_waitcnt lgkmcnt(5)
	v_pk_mul_f32 v[126:127], v[14:15], v[20:21]
	v_pk_mul_f32 v[128:129], v[14:15], v[112:113]
	v_pk_fma_f32 v[126:127], v[16:17], v[22:23], v[126:127]
	v_pk_fma_f32 v[128:129], v[16:17], v[114:115], v[128:129]
	v_add_f32_e32 v124, v126, v127
	v_pk_fma_f32 v[14:15], v[28:29], v[120:121], v[14:15] op_sel_hi:[1,0,1]
	v_add_f32_e32 v131, v128, v129
	v_add_f32_dpp v124, v124, v124 quad_perm:[1,0,3,2] row_mask:0xf bank_mask:0xf bound_ctrl:1
	v_pk_fma_f32 v[16:17], v[30:31], v[120:121], v[16:17] op_sel_hi:[1,0,1]
	ds_read_b128 v[52:55], v18 offset:1536
	v_add_f32_dpp v124, v124, v124 quad_perm:[2,3,0,1] row_mask:0xf bank_mask:0xf bound_ctrl:1
	ds_read_b128 v[60:63], v18 offset:26112
	ds_read2_b32 v[122:123], v2 offset0:96 offset1:112
	v_add_f32_dpp v124, v124, v124 row_half_mirror row_mask:0xf bank_mask:0xf bound_ctrl:1
	ds_read_b128 v[56:59], v18 offset:9728
	ds_read_b128 v[64:67], v18 offset:34304
	v_add_f32_dpp v124, v124, v124 row_mirror row_mask:0xf bank_mask:0xf bound_ctrl:1
	v_pk_fma_f32 v[14:15], v[24:25], v[124:125], v[14:15] op_sel_hi:[1,0,1] neg_lo:[0,1,0] neg_hi:[0,1,0]
	v_pk_fma_f32 v[16:17], v[26:27], v[124:125], v[16:17] op_sel_hi:[1,0,1] neg_lo:[0,1,0] neg_hi:[0,1,0]
	v_add_f32_dpp v133, v130, v130 row_mirror row_mask:0xf bank_mask:0x3 bound_ctrl:1
	s_waitcnt lgkmcnt(6)
	v_pk_mul_f32 v[126:127], v[14:15], v[36:37]
	v_pk_mul_f32 v[128:129], v[14:15], v[32:33]
	v_pk_fma_f32 v[126:127], v[16:17], v[38:39], v[126:127]
	v_pk_fma_f32 v[128:129], v[16:17], v[34:35], v[128:129]
	v_add_f32_e32 v124, v126, v127
	v_pk_fma_f32 v[14:15], v[44:45], v[120:121], v[14:15] op_sel:[0,1,0]
	v_add_f32_e32 v130, v128, v129
	v_add_f32_dpp v124, v124, v124 quad_perm:[1,0,3,2] row_mask:0xf bank_mask:0xf bound_ctrl:1
	v_pk_fma_f32 v[16:17], v[46:47], v[120:121], v[16:17] op_sel:[0,1,0]
	ds_read_b128 v[100:103], v18 offset:1792
	v_add_f32_dpp v124, v124, v124 quad_perm:[2,3,0,1] row_mask:0xf bank_mask:0xf bound_ctrl:1
	ds_read_b128 v[108:111], v18 offset:26368
	ds_read_b128 v[116:119], v18 offset:18176
	v_add_f32_dpp v124, v124, v124 row_half_mirror row_mask:0xf bank_mask:0xf bound_ctrl:1
	ds_read_b128 v[104:107], v18 offset:9984
	ds_read_b128 v[112:115], v18 offset:34560
	v_add_f32_dpp v124, v124, v124 row_mirror row_mask:0xf bank_mask:0xf bound_ctrl:1
	v_pk_fma_f32 v[14:15], v[40:41], v[124:125], v[14:15] op_sel_hi:[1,0,1] neg_lo:[0,1,0] neg_hi:[0,1,0]
	v_pk_fma_f32 v[16:17], v[42:43], v[124:125], v[16:17] op_sel_hi:[1,0,1] neg_lo:[0,1,0] neg_hi:[0,1,0]
	v_add_f32_dpp v133, v131, v131 row_mirror row_mask:0xf bank_mask:0xc bound_ctrl:1
	v_add_f32_dpp v134, v132, v132 row_half_mirror row_mask:0xf bank_mask:0x5 bound_ctrl:1
	s_waitcnt lgkmcnt(6)
	v_pk_mul_f32 v[126:127], v[14:15], v[52:53]
	v_pk_mul_f32 v[128:129], v[14:15], v[48:49]
	v_pk_fma_f32 v[126:127], v[16:17], v[54:55], v[126:127]
	v_pk_fma_f32 v[128:129], v[16:17], v[50:51], v[128:129]
	v_add_f32_e32 v124, v126, v127
	v_pk_fma_f32 v[14:15], v[60:61], v[122:123], v[14:15] op_sel_hi:[1,0,1]
	v_add_f32_e32 v131, v128, v129
	v_add_f32_dpp v124, v124, v124 quad_perm:[1,0,3,2] row_mask:0xf bank_mask:0xf bound_ctrl:1
	v_pk_fma_f32 v[16:17], v[62:63], v[122:123], v[16:17] op_sel_hi:[1,0,1]
	ds_read_b128 v[20:23], v18 offset:2048
	v_add_f32_dpp v124, v124, v124 quad_perm:[2,3,0,1] row_mask:0xf bank_mask:0xf bound_ctrl:1
	ds_read_b128 v[28:31], v18 offset:26624
	ds_read2_b32 v[120:121], v2 offset0:128 offset1:144
	v_add_f32_dpp v124, v124, v124 row_half_mirror row_mask:0xf bank_mask:0xf bound_ctrl:1
	ds_read_b128 v[24:27], v18 offset:10240
	ds_read_b128 v[32:35], v18 offset:34816
	v_add_f32_dpp v124, v124, v124 row_mirror row_mask:0xf bank_mask:0xf bound_ctrl:1
	v_pk_fma_f32 v[14:15], v[56:57], v[124:125], v[14:15] op_sel_hi:[1,0,1] neg_lo:[0,1,0] neg_hi:[0,1,0]
	v_pk_fma_f32 v[16:17], v[58:59], v[124:125], v[16:17] op_sel_hi:[1,0,1] neg_lo:[0,1,0] neg_hi:[0,1,0]
	v_add_f32_dpp v134, v133, v133 row_half_mirror row_mask:0xf bank_mask:0xa bound_ctrl:1
	v_add_f32_dpp v132, v130, v130 row_mirror row_mask:0xf bank_mask:0x3 bound_ctrl:1
	s_waitcnt lgkmcnt(6)
	v_pk_mul_f32 v[126:127], v[14:15], v[100:101]
	v_pk_mul_f32 v[128:129], v[14:15], v[64:65]
	v_pk_fma_f32 v[126:127], v[16:17], v[102:103], v[126:127]
	v_pk_fma_f32 v[128:129], v[16:17], v[66:67], v[128:129]
	v_add_f32_e32 v124, v126, v127
	v_pk_fma_f32 v[14:15], v[108:109], v[122:123], v[14:15] op_sel:[0,1,0]
	v_add_f32_e32 v130, v128, v129
	v_add_f32_dpp v124, v124, v124 quad_perm:[1,0,3,2] row_mask:0xf bank_mask:0xf bound_ctrl:1
	v_pk_fma_f32 v[16:17], v[110:111], v[122:123], v[16:17] op_sel:[0,1,0]
	ds_read_b128 v[36:39], v18 offset:2304
	v_add_f32_dpp v124, v124, v124 quad_perm:[2,3,0,1] row_mask:0xf bank_mask:0xf bound_ctrl:1
	ds_read_b128 v[44:47], v18 offset:26880
	ds_read_b128 v[40:43], v18 offset:10496
	v_add_f32_dpp v124, v124, v124 row_half_mirror row_mask:0xf bank_mask:0xf bound_ctrl:1
	ds_read_b128 v[48:51], v18 offset:35072
	v_add_f32_dpp v132, v131, v131 row_mirror row_mask:0xf bank_mask:0xc bound_ctrl:1
	v_add_f32_dpp v124, v124, v124 row_mirror row_mask:0xf bank_mask:0xf bound_ctrl:1
	v_pk_fma_f32 v[14:15], v[104:105], v[124:125], v[14:15] op_sel_hi:[1,0,1] neg_lo:[0,1,0] neg_hi:[0,1,0]
	v_pk_fma_f32 v[16:17], v[106:107], v[124:125], v[16:17] op_sel_hi:[1,0,1] neg_lo:[0,1,0] neg_hi:[0,1,0]
	v_pk_mul_f32 v[14:15], v[14:15], v[116:117]
	v_pk_mul_f32 v[16:17], v[16:17], v[118:119]
	s_waitcnt lgkmcnt(5)
	v_pk_mul_f32 v[126:127], v[14:15], v[20:21]
	v_pk_mul_f32 v[128:129], v[14:15], v[112:113]
	v_pk_fma_f32 v[126:127], v[16:17], v[22:23], v[126:127]
	v_pk_fma_f32 v[128:129], v[16:17], v[114:115], v[128:129]
	v_add_f32_e32 v124, v126, v127
	v_pk_fma_f32 v[14:15], v[28:29], v[120:121], v[14:15] op_sel_hi:[1,0,1]
	v_add_f32_e32 v131, v128, v129
	v_add_f32_dpp v124, v124, v124 quad_perm:[1,0,3,2] row_mask:0xf bank_mask:0xf bound_ctrl:1
	v_pk_fma_f32 v[16:17], v[30:31], v[120:121], v[16:17] op_sel_hi:[1,0,1]
	ds_read_b128 v[52:55], v18 offset:2560
	v_add_f32_dpp v124, v124, v124 quad_perm:[2,3,0,1] row_mask:0xf bank_mask:0xf bound_ctrl:1
	ds_read_b128 v[60:63], v18 offset:27136
	ds_read2_b32 v[122:123], v2 offset0:160 offset1:176
	v_add_f32_dpp v124, v124, v124 row_half_mirror row_mask:0xf bank_mask:0xf bound_ctrl:1
	ds_read_b128 v[56:59], v18 offset:10752
	ds_read_b128 v[64:67], v18 offset:35328
	v_add_f32_dpp v124, v124, v124 row_mirror row_mask:0xf bank_mask:0xf bound_ctrl:1
	v_pk_fma_f32 v[14:15], v[24:25], v[124:125], v[14:15] op_sel_hi:[1,0,1] neg_lo:[0,1,0] neg_hi:[0,1,0]
	v_pk_fma_f32 v[16:17], v[26:27], v[124:125], v[16:17] op_sel_hi:[1,0,1] neg_lo:[0,1,0] neg_hi:[0,1,0]
	v_add_f32_dpp v133, v130, v130 row_mirror row_mask:0xf bank_mask:0x3 bound_ctrl:1
	s_waitcnt lgkmcnt(6)
	v_pk_mul_f32 v[126:127], v[14:15], v[36:37]
	v_pk_mul_f32 v[128:129], v[14:15], v[32:33]
	v_pk_fma_f32 v[126:127], v[16:17], v[38:39], v[126:127]
	v_pk_fma_f32 v[128:129], v[16:17], v[34:35], v[128:129]
	v_add_f32_e32 v124, v126, v127
	v_pk_fma_f32 v[14:15], v[44:45], v[120:121], v[14:15] op_sel:[0,1,0]
	v_add_f32_e32 v130, v128, v129
	v_add_f32_dpp v124, v124, v124 quad_perm:[1,0,3,2] row_mask:0xf bank_mask:0xf bound_ctrl:1
	v_pk_fma_f32 v[16:17], v[46:47], v[120:121], v[16:17] op_sel:[0,1,0]
	ds_read_b128 v[100:103], v18 offset:2816
	v_add_f32_dpp v124, v124, v124 quad_perm:[2,3,0,1] row_mask:0xf bank_mask:0xf bound_ctrl:1
	ds_read_b128 v[108:111], v18 offset:27392
	ds_read_b128 v[116:119], v18 offset:19200
	v_add_f32_dpp v124, v124, v124 row_half_mirror row_mask:0xf bank_mask:0xf bound_ctrl:1
	ds_read_b128 v[104:107], v18 offset:11008
	ds_read_b128 v[112:115], v18 offset:35584
	v_add_f32_dpp v124, v124, v124 row_mirror row_mask:0xf bank_mask:0xf bound_ctrl:1
	v_pk_fma_f32 v[14:15], v[40:41], v[124:125], v[14:15] op_sel_hi:[1,0,1] neg_lo:[0,1,0] neg_hi:[0,1,0]
	v_pk_fma_f32 v[16:17], v[42:43], v[124:125], v[16:17] op_sel_hi:[1,0,1] neg_lo:[0,1,0] neg_hi:[0,1,0]
	v_add_f32_dpp v133, v131, v131 row_mirror row_mask:0xf bank_mask:0xc bound_ctrl:1
	v_add_f32_dpp v135, v132, v132 row_half_mirror row_mask:0xf bank_mask:0x5 bound_ctrl:1
	s_waitcnt lgkmcnt(6)
	v_pk_mul_f32 v[126:127], v[14:15], v[52:53]
	v_pk_mul_f32 v[128:129], v[14:15], v[48:49]
	v_pk_fma_f32 v[126:127], v[16:17], v[54:55], v[126:127]
	v_pk_fma_f32 v[128:129], v[16:17], v[50:51], v[128:129]
	v_add_f32_e32 v124, v126, v127
	v_pk_fma_f32 v[14:15], v[60:61], v[122:123], v[14:15] op_sel_hi:[1,0,1]
	v_add_f32_e32 v131, v128, v129
	v_add_f32_dpp v124, v124, v124 quad_perm:[1,0,3,2] row_mask:0xf bank_mask:0xf bound_ctrl:1
	v_pk_fma_f32 v[16:17], v[62:63], v[122:123], v[16:17] op_sel_hi:[1,0,1]
	ds_read_b128 v[20:23], v18 offset:3072
	v_add_f32_dpp v124, v124, v124 quad_perm:[2,3,0,1] row_mask:0xf bank_mask:0xf bound_ctrl:1
	ds_read_b128 v[28:31], v18 offset:27648
	ds_read2_b32 v[120:121], v2 offset0:192 offset1:208
	v_add_f32_dpp v124, v124, v124 row_half_mirror row_mask:0xf bank_mask:0xf bound_ctrl:1
	ds_read_b128 v[24:27], v18 offset:11264
	ds_read_b128 v[32:35], v18 offset:35840
	v_add_f32_dpp v124, v124, v124 row_mirror row_mask:0xf bank_mask:0xf bound_ctrl:1
	v_pk_fma_f32 v[14:15], v[56:57], v[124:125], v[14:15] op_sel_hi:[1,0,1] neg_lo:[0,1,0] neg_hi:[0,1,0]
	v_pk_fma_f32 v[16:17], v[58:59], v[124:125], v[16:17] op_sel_hi:[1,0,1] neg_lo:[0,1,0] neg_hi:[0,1,0]
	v_add_f32_dpp v135, v133, v133 row_half_mirror row_mask:0xf bank_mask:0xa bound_ctrl:1
	v_add_f32_dpp v138, v134, v134 quad_perm:[2,3,0,1] row_mask:0xf bank_mask:0xf bound_ctrl:1
	s_nop 0
	v_add_f32_dpp v98, v135, v135 quad_perm:[2,3,0,1] row_mask:0xf bank_mask:0xf bound_ctrl:1
	v_cndmask_b32_e64 v136, v138, v98, s[14:15]
	v_add_f32_dpp v132, v130, v130 row_mirror row_mask:0xf bank_mask:0x3 bound_ctrl:1
	s_waitcnt lgkmcnt(6)
	v_pk_mul_f32 v[126:127], v[14:15], v[100:101]
	v_pk_mul_f32 v[128:129], v[14:15], v[64:65]
	v_pk_fma_f32 v[126:127], v[16:17], v[102:103], v[126:127]
	v_pk_fma_f32 v[128:129], v[16:17], v[66:67], v[128:129]
	v_add_f32_e32 v124, v126, v127
	v_pk_fma_f32 v[14:15], v[108:109], v[122:123], v[14:15] op_sel:[0,1,0]
	v_add_f32_e32 v130, v128, v129
	v_add_f32_dpp v124, v124, v124 quad_perm:[1,0,3,2] row_mask:0xf bank_mask:0xf bound_ctrl:1
	v_pk_fma_f32 v[16:17], v[110:111], v[122:123], v[16:17] op_sel:[0,1,0]
	ds_read_b128 v[36:39], v18 offset:3328
	v_add_f32_dpp v124, v124, v124 quad_perm:[2,3,0,1] row_mask:0xf bank_mask:0xf bound_ctrl:1
	ds_read_b128 v[44:47], v18 offset:27904
	ds_read_b128 v[40:43], v18 offset:11520
	v_add_f32_dpp v124, v124, v124 row_half_mirror row_mask:0xf bank_mask:0xf bound_ctrl:1
	ds_read_b128 v[48:51], v18 offset:36096
	v_add_f32_dpp v132, v131, v131 row_mirror row_mask:0xf bank_mask:0xc bound_ctrl:1
	v_add_f32_dpp v124, v124, v124 row_mirror row_mask:0xf bank_mask:0xf bound_ctrl:1
	v_pk_fma_f32 v[14:15], v[104:105], v[124:125], v[14:15] op_sel_hi:[1,0,1] neg_lo:[0,1,0] neg_hi:[0,1,0]
	v_pk_fma_f32 v[16:17], v[106:107], v[124:125], v[16:17] op_sel_hi:[1,0,1] neg_lo:[0,1,0] neg_hi:[0,1,0]
	v_pk_mul_f32 v[14:15], v[14:15], v[116:117]
	v_pk_mul_f32 v[16:17], v[16:17], v[118:119]
	s_waitcnt lgkmcnt(5)
	v_pk_mul_f32 v[126:127], v[14:15], v[20:21]
	v_pk_mul_f32 v[128:129], v[14:15], v[112:113]
	v_pk_fma_f32 v[126:127], v[16:17], v[22:23], v[126:127]
	v_pk_fma_f32 v[128:129], v[16:17], v[114:115], v[128:129]
	v_add_f32_e32 v124, v126, v127
	v_pk_fma_f32 v[14:15], v[28:29], v[120:121], v[14:15] op_sel_hi:[1,0,1]
	v_add_f32_e32 v131, v128, v129
	v_add_f32_dpp v124, v124, v124 quad_perm:[1,0,3,2] row_mask:0xf bank_mask:0xf bound_ctrl:1
	v_pk_fma_f32 v[16:17], v[30:31], v[120:121], v[16:17] op_sel_hi:[1,0,1]
	ds_read_b128 v[52:55], v18 offset:3584
	v_add_f32_dpp v124, v124, v124 quad_perm:[2,3,0,1] row_mask:0xf bank_mask:0xf bound_ctrl:1
	ds_read_b128 v[60:63], v18 offset:28160
	ds_read2_b32 v[122:123], v2 offset0:224 offset1:240
	v_add_f32_dpp v124, v124, v124 row_half_mirror row_mask:0xf bank_mask:0xf bound_ctrl:1
	ds_read_b128 v[56:59], v18 offset:11776
	ds_read_b128 v[64:67], v18 offset:36352
	v_add_f32_dpp v124, v124, v124 row_mirror row_mask:0xf bank_mask:0xf bound_ctrl:1
	v_pk_fma_f32 v[14:15], v[24:25], v[124:125], v[14:15] op_sel_hi:[1,0,1] neg_lo:[0,1,0] neg_hi:[0,1,0]
	v_pk_fma_f32 v[16:17], v[26:27], v[124:125], v[16:17] op_sel_hi:[1,0,1] neg_lo:[0,1,0] neg_hi:[0,1,0]
	v_mul_hi_i32_i24_e32 v9, s44, v94
	v_mul_i32_i24_e32 v8, s44, v94
	v_add_f32_dpp v133, v130, v130 row_mirror row_mask:0xf bank_mask:0x3 bound_ctrl:1
	s_waitcnt lgkmcnt(6)
	v_pk_mul_f32 v[126:127], v[14:15], v[36:37]
	v_pk_mul_f32 v[128:129], v[14:15], v[32:33]
	v_pk_fma_f32 v[126:127], v[16:17], v[38:39], v[126:127]
	v_pk_fma_f32 v[128:129], v[16:17], v[34:35], v[128:129]
	v_add_f32_e32 v124, v126, v127
	v_pk_fma_f32 v[14:15], v[44:45], v[120:121], v[14:15] op_sel:[0,1,0]
	v_add_f32_e32 v130, v128, v129
	v_add_f32_dpp v124, v124, v124 quad_perm:[1,0,3,2] row_mask:0xf bank_mask:0xf bound_ctrl:1
	v_pk_fma_f32 v[16:17], v[46:47], v[120:121], v[16:17] op_sel:[0,1,0]
	ds_read_b128 v[100:103], v18 offset:3840
	v_add_f32_dpp v124, v124, v124 quad_perm:[2,3,0,1] row_mask:0xf bank_mask:0xf bound_ctrl:1
	ds_read_b128 v[108:111], v18 offset:28416
	ds_read_b128 v[116:119], v18 offset:20224
	v_add_f32_dpp v124, v124, v124 row_half_mirror row_mask:0xf bank_mask:0xf bound_ctrl:1
	ds_read_b128 v[104:107], v18 offset:12032
	ds_read_b128 v[112:115], v18 offset:36608
	v_add_f32_dpp v124, v124, v124 row_mirror row_mask:0xf bank_mask:0xf bound_ctrl:1
	v_pk_fma_f32 v[14:15], v[40:41], v[124:125], v[14:15] op_sel_hi:[1,0,1] neg_lo:[0,1,0] neg_hi:[0,1,0]
	v_pk_fma_f32 v[16:17], v[42:43], v[124:125], v[16:17] op_sel_hi:[1,0,1] neg_lo:[0,1,0] neg_hi:[0,1,0]
	v_lshl_add_u64 v[8:9], v[8:9], 1, v[12:13]
	v_add_f32_dpp v133, v131, v131 row_mirror row_mask:0xf bank_mask:0xc bound_ctrl:1
	v_add_f32_dpp v134, v132, v132 row_half_mirror row_mask:0xf bank_mask:0x5 bound_ctrl:1
	s_waitcnt lgkmcnt(6)
	v_pk_mul_f32 v[126:127], v[14:15], v[52:53]
	v_pk_mul_f32 v[128:129], v[14:15], v[48:49]
	v_pk_fma_f32 v[126:127], v[16:17], v[54:55], v[126:127]
	v_pk_fma_f32 v[128:129], v[16:17], v[50:51], v[128:129]
	v_add_f32_e32 v124, v126, v127
	v_pk_fma_f32 v[14:15], v[60:61], v[122:123], v[14:15] op_sel_hi:[1,0,1]
	v_add_f32_e32 v131, v128, v129
	v_add_f32_dpp v124, v124, v124 quad_perm:[1,0,3,2] row_mask:0xf bank_mask:0xf bound_ctrl:1
	v_pk_fma_f32 v[16:17], v[62:63], v[122:123], v[16:17] op_sel_hi:[1,0,1]
	ds_read_b128 v[20:23], v18 offset:4096
	v_add_f32_dpp v124, v124, v124 quad_perm:[2,3,0,1] row_mask:0xf bank_mask:0xf bound_ctrl:1
	ds_read_b128 v[28:31], v18 offset:28672
	ds_read2_b32 v[120:121], v3 offset1:16
	v_add_f32_dpp v124, v124, v124 row_half_mirror row_mask:0xf bank_mask:0xf bound_ctrl:1
	ds_read_b128 v[24:27], v18 offset:12288
	ds_read_b128 v[32:35], v18 offset:36864
	v_add_f32_dpp v124, v124, v124 row_mirror row_mask:0xf bank_mask:0xf bound_ctrl:1
	v_pk_fma_f32 v[14:15], v[56:57], v[124:125], v[14:15] op_sel_hi:[1,0,1] neg_lo:[0,1,0] neg_hi:[0,1,0]
	v_pk_fma_f32 v[16:17], v[58:59], v[124:125], v[16:17] op_sel_hi:[1,0,1] neg_lo:[0,1,0] neg_hi:[0,1,0]
	v_add_f32_dpp v134, v133, v133 row_half_mirror row_mask:0xf bank_mask:0xa bound_ctrl:1
	v_add_f32_dpp v132, v130, v130 row_mirror row_mask:0xf bank_mask:0x3 bound_ctrl:1
	s_waitcnt lgkmcnt(6)
	v_pk_mul_f32 v[126:127], v[14:15], v[100:101]
	v_pk_mul_f32 v[128:129], v[14:15], v[64:65]
	v_pk_fma_f32 v[126:127], v[16:17], v[102:103], v[126:127]
	v_pk_fma_f32 v[128:129], v[16:17], v[66:67], v[128:129]
	v_add_f32_e32 v124, v126, v127
	v_pk_fma_f32 v[14:15], v[108:109], v[122:123], v[14:15] op_sel:[0,1,0]
	v_add_f32_e32 v130, v128, v129
	v_add_f32_dpp v124, v124, v124 quad_perm:[1,0,3,2] row_mask:0xf bank_mask:0xf bound_ctrl:1
	v_pk_fma_f32 v[16:17], v[110:111], v[122:123], v[16:17] op_sel:[0,1,0]
	ds_read_b128 v[36:39], v18 offset:4352
	v_add_f32_dpp v124, v124, v124 quad_perm:[2,3,0,1] row_mask:0xf bank_mask:0xf bound_ctrl:1
	ds_read_b128 v[44:47], v18 offset:28928
	ds_read_b128 v[40:43], v18 offset:12544
	v_add_f32_dpp v124, v124, v124 row_half_mirror row_mask:0xf bank_mask:0xf bound_ctrl:1
	ds_read_b128 v[48:51], v18 offset:37120
	v_add_f32_dpp v132, v131, v131 row_mirror row_mask:0xf bank_mask:0xc bound_ctrl:1
	v_add_f32_dpp v124, v124, v124 row_mirror row_mask:0xf bank_mask:0xf bound_ctrl:1
	v_pk_fma_f32 v[14:15], v[104:105], v[124:125], v[14:15] op_sel_hi:[1,0,1] neg_lo:[0,1,0] neg_hi:[0,1,0]
	v_pk_fma_f32 v[16:17], v[106:107], v[124:125], v[16:17] op_sel_hi:[1,0,1] neg_lo:[0,1,0] neg_hi:[0,1,0]
	v_pk_mul_f32 v[14:15], v[14:15], v[116:117]
	v_pk_mul_f32 v[16:17], v[16:17], v[118:119]
	s_waitcnt lgkmcnt(5)
	v_pk_mul_f32 v[126:127], v[14:15], v[20:21]
	v_pk_mul_f32 v[128:129], v[14:15], v[112:113]
	v_pk_fma_f32 v[126:127], v[16:17], v[22:23], v[126:127]
	v_pk_fma_f32 v[128:129], v[16:17], v[114:115], v[128:129]
	v_add_f32_e32 v124, v126, v127
	v_pk_fma_f32 v[14:15], v[28:29], v[120:121], v[14:15] op_sel_hi:[1,0,1]
	v_add_f32_e32 v131, v128, v129
	v_add_f32_dpp v124, v124, v124 quad_perm:[1,0,3,2] row_mask:0xf bank_mask:0xf bound_ctrl:1
	v_pk_fma_f32 v[16:17], v[30:31], v[120:121], v[16:17] op_sel_hi:[1,0,1]
	ds_read_b128 v[52:55], v18 offset:4608
	v_add_f32_dpp v124, v124, v124 quad_perm:[2,3,0,1] row_mask:0xf bank_mask:0xf bound_ctrl:1
	ds_read_b128 v[60:63], v18 offset:29184
	ds_read2_b32 v[122:123], v3 offset0:32 offset1:48
	v_add_f32_dpp v124, v124, v124 row_half_mirror row_mask:0xf bank_mask:0xf bound_ctrl:1
	ds_read_b128 v[56:59], v18 offset:12800
	ds_read_b128 v[64:67], v18 offset:37376
	v_add_f32_dpp v124, v124, v124 row_mirror row_mask:0xf bank_mask:0xf bound_ctrl:1
	v_pk_fma_f32 v[14:15], v[24:25], v[124:125], v[14:15] op_sel_hi:[1,0,1] neg_lo:[0,1,0] neg_hi:[0,1,0]
	v_pk_fma_f32 v[16:17], v[26:27], v[124:125], v[16:17] op_sel_hi:[1,0,1] neg_lo:[0,1,0] neg_hi:[0,1,0]
	v_add_f32_dpp v133, v130, v130 row_mirror row_mask:0xf bank_mask:0x3 bound_ctrl:1
	s_waitcnt lgkmcnt(6)
	v_pk_mul_f32 v[126:127], v[14:15], v[36:37]
	v_pk_mul_f32 v[128:129], v[14:15], v[32:33]
	v_pk_fma_f32 v[126:127], v[16:17], v[38:39], v[126:127]
	v_pk_fma_f32 v[128:129], v[16:17], v[34:35], v[128:129]
	v_add_f32_e32 v124, v126, v127
	v_pk_fma_f32 v[14:15], v[44:45], v[120:121], v[14:15] op_sel:[0,1,0]
	v_add_f32_e32 v130, v128, v129
	v_add_f32_dpp v124, v124, v124 quad_perm:[1,0,3,2] row_mask:0xf bank_mask:0xf bound_ctrl:1
	v_pk_fma_f32 v[16:17], v[46:47], v[120:121], v[16:17] op_sel:[0,1,0]
	ds_read_b128 v[100:103], v18 offset:4864
	v_add_f32_dpp v124, v124, v124 quad_perm:[2,3,0,1] row_mask:0xf bank_mask:0xf bound_ctrl:1
	ds_read_b128 v[108:111], v18 offset:29440
	ds_read_b128 v[116:119], v18 offset:21248
	v_add_f32_dpp v124, v124, v124 row_half_mirror row_mask:0xf bank_mask:0xf bound_ctrl:1
	ds_read_b128 v[104:107], v18 offset:13056
	ds_read_b128 v[112:115], v18 offset:37632
	v_add_f32_dpp v124, v124, v124 row_mirror row_mask:0xf bank_mask:0xf bound_ctrl:1
	v_pk_fma_f32 v[14:15], v[40:41], v[124:125], v[14:15] op_sel_hi:[1,0,1] neg_lo:[0,1,0] neg_hi:[0,1,0]
	v_pk_fma_f32 v[16:17], v[42:43], v[124:125], v[16:17] op_sel_hi:[1,0,1] neg_lo:[0,1,0] neg_hi:[0,1,0]
	v_add_f32_dpp v133, v131, v131 row_mirror row_mask:0xf bank_mask:0xc bound_ctrl:1
	v_add_f32_dpp v135, v132, v132 row_half_mirror row_mask:0xf bank_mask:0x5 bound_ctrl:1
	s_waitcnt lgkmcnt(6)
	v_pk_mul_f32 v[126:127], v[14:15], v[52:53]
	v_pk_mul_f32 v[128:129], v[14:15], v[48:49]
	v_pk_fma_f32 v[126:127], v[16:17], v[54:55], v[126:127]
	v_pk_fma_f32 v[128:129], v[16:17], v[50:51], v[128:129]
	v_add_f32_e32 v124, v126, v127
	v_pk_fma_f32 v[14:15], v[60:61], v[122:123], v[14:15] op_sel_hi:[1,0,1]
	v_add_f32_e32 v131, v128, v129
	v_add_f32_dpp v124, v124, v124 quad_perm:[1,0,3,2] row_mask:0xf bank_mask:0xf bound_ctrl:1
	v_pk_fma_f32 v[16:17], v[62:63], v[122:123], v[16:17] op_sel_hi:[1,0,1]
	ds_read_b128 v[20:23], v18 offset:5120
	v_add_f32_dpp v124, v124, v124 quad_perm:[2,3,0,1] row_mask:0xf bank_mask:0xf bound_ctrl:1
	ds_read_b128 v[28:31], v18 offset:29696
	ds_read2_b32 v[120:121], v3 offset0:64 offset1:80
	v_add_f32_dpp v124, v124, v124 row_half_mirror row_mask:0xf bank_mask:0xf bound_ctrl:1
	ds_read_b128 v[24:27], v18 offset:13312
	ds_read_b128 v[32:35], v18 offset:37888
	v_add_f32_dpp v124, v124, v124 row_mirror row_mask:0xf bank_mask:0xf bound_ctrl:1
	v_pk_fma_f32 v[14:15], v[56:57], v[124:125], v[14:15] op_sel_hi:[1,0,1] neg_lo:[0,1,0] neg_hi:[0,1,0]
	v_pk_fma_f32 v[16:17], v[58:59], v[124:125], v[16:17] op_sel_hi:[1,0,1] neg_lo:[0,1,0] neg_hi:[0,1,0]
	v_add_f32_dpp v135, v133, v133 row_half_mirror row_mask:0xf bank_mask:0xa bound_ctrl:1
	v_add_f32_dpp v138, v134, v134 quad_perm:[2,3,0,1] row_mask:0xf bank_mask:0xf bound_ctrl:1
	s_nop 0
	v_add_f32_dpp v98, v135, v135 quad_perm:[2,3,0,1] row_mask:0xf bank_mask:0xf bound_ctrl:1
	v_cndmask_b32_e64 v137, v138, v98, s[14:15]
	v_add_f32_dpp v138, v136, v136 quad_perm:[1,0,3,2] row_mask:0xf bank_mask:0xf bound_ctrl:1
	s_nop 0
	v_add_f32_dpp v98, v137, v137 quad_perm:[1,0,3,2] row_mask:0xf bank_mask:0xf bound_ctrl:1
	v_cndmask_b32_e64 v99, v138, v98, s[16:17]
	v_bfe_u32 v6, v99, 16, 1
	v_add3_u32 v6, v99, v6, s3
	global_store_short_d16_hi v[4:5], v6, off
	v_add_f32_dpp v132, v130, v130 row_mirror row_mask:0xf bank_mask:0x3 bound_ctrl:1
	s_waitcnt lgkmcnt(6)
	v_pk_mul_f32 v[126:127], v[14:15], v[100:101]
	v_pk_mul_f32 v[128:129], v[14:15], v[64:65]
	v_pk_fma_f32 v[126:127], v[16:17], v[102:103], v[126:127]
	v_pk_fma_f32 v[128:129], v[16:17], v[66:67], v[128:129]
	v_add_f32_e32 v124, v126, v127
	v_pk_fma_f32 v[14:15], v[108:109], v[122:123], v[14:15] op_sel:[0,1,0]
	v_add_f32_e32 v130, v128, v129
	v_add_f32_dpp v124, v124, v124 quad_perm:[1,0,3,2] row_mask:0xf bank_mask:0xf bound_ctrl:1
	v_pk_fma_f32 v[16:17], v[110:111], v[122:123], v[16:17] op_sel:[0,1,0]
	ds_read_b128 v[36:39], v18 offset:5376
	v_add_f32_dpp v124, v124, v124 quad_perm:[2,3,0,1] row_mask:0xf bank_mask:0xf bound_ctrl:1
	ds_read_b128 v[44:47], v18 offset:29952
	ds_read_b128 v[40:43], v18 offset:13568
	v_add_f32_dpp v124, v124, v124 row_half_mirror row_mask:0xf bank_mask:0xf bound_ctrl:1
	ds_read_b128 v[48:51], v18 offset:38144
	v_add_f32_dpp v132, v131, v131 row_mirror row_mask:0xf bank_mask:0xc bound_ctrl:1
	v_add_f32_dpp v124, v124, v124 row_mirror row_mask:0xf bank_mask:0xf bound_ctrl:1
	v_pk_fma_f32 v[14:15], v[104:105], v[124:125], v[14:15] op_sel_hi:[1,0,1] neg_lo:[0,1,0] neg_hi:[0,1,0]
	v_pk_fma_f32 v[16:17], v[106:107], v[124:125], v[16:17] op_sel_hi:[1,0,1] neg_lo:[0,1,0] neg_hi:[0,1,0]
	v_pk_mul_f32 v[14:15], v[14:15], v[116:117]
	v_pk_mul_f32 v[16:17], v[16:17], v[118:119]
	s_waitcnt lgkmcnt(5)
	v_pk_mul_f32 v[126:127], v[14:15], v[20:21]
	v_pk_mul_f32 v[128:129], v[14:15], v[112:113]
	v_pk_fma_f32 v[126:127], v[16:17], v[22:23], v[126:127]
	v_pk_fma_f32 v[128:129], v[16:17], v[114:115], v[128:129]
	v_add_f32_e32 v124, v126, v127
	v_pk_fma_f32 v[14:15], v[28:29], v[120:121], v[14:15] op_sel_hi:[1,0,1]
	v_add_f32_e32 v131, v128, v129
	v_add_f32_dpp v124, v124, v124 quad_perm:[1,0,3,2] row_mask:0xf bank_mask:0xf bound_ctrl:1
	v_pk_fma_f32 v[16:17], v[30:31], v[120:121], v[16:17] op_sel_hi:[1,0,1]
	ds_read_b128 v[52:55], v18 offset:5632
	v_add_f32_dpp v124, v124, v124 quad_perm:[2,3,0,1] row_mask:0xf bank_mask:0xf bound_ctrl:1
	ds_read_b128 v[60:63], v18 offset:30208
	ds_read2_b32 v[122:123], v3 offset0:96 offset1:112
	v_add_f32_dpp v124, v124, v124 row_half_mirror row_mask:0xf bank_mask:0xf bound_ctrl:1
	ds_read_b128 v[56:59], v18 offset:13824
	ds_read_b128 v[64:67], v18 offset:38400
	v_add_f32_dpp v124, v124, v124 row_mirror row_mask:0xf bank_mask:0xf bound_ctrl:1
	v_pk_fma_f32 v[14:15], v[24:25], v[124:125], v[14:15] op_sel_hi:[1,0,1] neg_lo:[0,1,0] neg_hi:[0,1,0]
	v_pk_fma_f32 v[16:17], v[26:27], v[124:125], v[16:17] op_sel_hi:[1,0,1] neg_lo:[0,1,0] neg_hi:[0,1,0]
	v_add_f32_dpp v133, v130, v130 row_mirror row_mask:0xf bank_mask:0x3 bound_ctrl:1
	s_waitcnt lgkmcnt(6)
	v_pk_mul_f32 v[126:127], v[14:15], v[36:37]
	v_pk_mul_f32 v[128:129], v[14:15], v[32:33]
	v_pk_fma_f32 v[126:127], v[16:17], v[38:39], v[126:127]
	v_pk_fma_f32 v[128:129], v[16:17], v[34:35], v[128:129]
	v_add_f32_e32 v124, v126, v127
	v_pk_fma_f32 v[14:15], v[44:45], v[120:121], v[14:15] op_sel:[0,1,0]
	v_add_f32_e32 v130, v128, v129
	v_add_f32_dpp v124, v124, v124 quad_perm:[1,0,3,2] row_mask:0xf bank_mask:0xf bound_ctrl:1
	v_pk_fma_f32 v[16:17], v[46:47], v[120:121], v[16:17] op_sel:[0,1,0]
	ds_read_b128 v[100:103], v18 offset:5888
	v_add_f32_dpp v124, v124, v124 quad_perm:[2,3,0,1] row_mask:0xf bank_mask:0xf bound_ctrl:1
	ds_read_b128 v[108:111], v18 offset:30464
	ds_read_b128 v[116:119], v18 offset:22272
	v_add_f32_dpp v124, v124, v124 row_half_mirror row_mask:0xf bank_mask:0xf bound_ctrl:1
	ds_read_b128 v[104:107], v18 offset:14080
	ds_read_b128 v[112:115], v18 offset:38656
	v_add_f32_dpp v124, v124, v124 row_mirror row_mask:0xf bank_mask:0xf bound_ctrl:1
	v_pk_fma_f32 v[14:15], v[40:41], v[124:125], v[14:15] op_sel_hi:[1,0,1] neg_lo:[0,1,0] neg_hi:[0,1,0]
	v_pk_fma_f32 v[16:17], v[42:43], v[124:125], v[16:17] op_sel_hi:[1,0,1] neg_lo:[0,1,0] neg_hi:[0,1,0]
	v_add_f32_dpp v133, v131, v131 row_mirror row_mask:0xf bank_mask:0xc bound_ctrl:1
	v_add_f32_dpp v134, v132, v132 row_half_mirror row_mask:0xf bank_mask:0x5 bound_ctrl:1
	s_waitcnt lgkmcnt(6)
	v_pk_mul_f32 v[126:127], v[14:15], v[52:53]
	v_pk_mul_f32 v[128:129], v[14:15], v[48:49]
	v_pk_fma_f32 v[126:127], v[16:17], v[54:55], v[126:127]
	v_pk_fma_f32 v[128:129], v[16:17], v[50:51], v[128:129]
	v_add_f32_e32 v124, v126, v127
	v_pk_fma_f32 v[14:15], v[60:61], v[122:123], v[14:15] op_sel_hi:[1,0,1]
	v_add_f32_e32 v131, v128, v129
	v_add_f32_dpp v124, v124, v124 quad_perm:[1,0,3,2] row_mask:0xf bank_mask:0xf bound_ctrl:1
	v_pk_fma_f32 v[16:17], v[62:63], v[122:123], v[16:17] op_sel_hi:[1,0,1]
	ds_read_b128 v[20:23], v18 offset:6144
	v_add_f32_dpp v124, v124, v124 quad_perm:[2,3,0,1] row_mask:0xf bank_mask:0xf bound_ctrl:1
	ds_read_b128 v[28:31], v18 offset:30720
	ds_read2_b32 v[120:121], v3 offset0:128 offset1:144
	v_add_f32_dpp v124, v124, v124 row_half_mirror row_mask:0xf bank_mask:0xf bound_ctrl:1
	ds_read_b128 v[24:27], v18 offset:14336
	ds_read_b128 v[32:35], v18 offset:38912
	v_add_f32_dpp v124, v124, v124 row_mirror row_mask:0xf bank_mask:0xf bound_ctrl:1
	v_pk_fma_f32 v[14:15], v[56:57], v[124:125], v[14:15] op_sel_hi:[1,0,1] neg_lo:[0,1,0] neg_hi:[0,1,0]
	v_pk_fma_f32 v[16:17], v[58:59], v[124:125], v[16:17] op_sel_hi:[1,0,1] neg_lo:[0,1,0] neg_hi:[0,1,0]
	v_add_f32_dpp v134, v133, v133 row_half_mirror row_mask:0xf bank_mask:0xa bound_ctrl:1
	v_add_f32_dpp v132, v130, v130 row_mirror row_mask:0xf bank_mask:0x3 bound_ctrl:1
	s_waitcnt lgkmcnt(6)
	v_pk_mul_f32 v[126:127], v[14:15], v[100:101]
	v_pk_mul_f32 v[128:129], v[14:15], v[64:65]
	v_pk_fma_f32 v[126:127], v[16:17], v[102:103], v[126:127]
	v_pk_fma_f32 v[128:129], v[16:17], v[66:67], v[128:129]
	v_add_f32_e32 v124, v126, v127
	v_pk_fma_f32 v[14:15], v[108:109], v[122:123], v[14:15] op_sel:[0,1,0]
	v_add_f32_e32 v130, v128, v129
	v_add_f32_dpp v124, v124, v124 quad_perm:[1,0,3,2] row_mask:0xf bank_mask:0xf bound_ctrl:1
	v_pk_fma_f32 v[16:17], v[110:111], v[122:123], v[16:17] op_sel:[0,1,0]
	ds_read_b128 v[36:39], v18 offset:6400
	v_add_f32_dpp v124, v124, v124 quad_perm:[2,3,0,1] row_mask:0xf bank_mask:0xf bound_ctrl:1
	ds_read_b128 v[44:47], v18 offset:30976
	ds_read_b128 v[40:43], v18 offset:14592
	v_add_f32_dpp v124, v124, v124 row_half_mirror row_mask:0xf bank_mask:0xf bound_ctrl:1
	ds_read_b128 v[48:51], v18 offset:39168
	v_add_f32_dpp v132, v131, v131 row_mirror row_mask:0xf bank_mask:0xc bound_ctrl:1
	v_add_f32_dpp v124, v124, v124 row_mirror row_mask:0xf bank_mask:0xf bound_ctrl:1
	v_pk_fma_f32 v[14:15], v[104:105], v[124:125], v[14:15] op_sel_hi:[1,0,1] neg_lo:[0,1,0] neg_hi:[0,1,0]
	v_pk_fma_f32 v[16:17], v[106:107], v[124:125], v[16:17] op_sel_hi:[1,0,1] neg_lo:[0,1,0] neg_hi:[0,1,0]
	v_pk_mul_f32 v[14:15], v[14:15], v[116:117]
	v_pk_mul_f32 v[16:17], v[16:17], v[118:119]
	s_waitcnt lgkmcnt(5)
	v_pk_mul_f32 v[126:127], v[14:15], v[20:21]
	v_pk_mul_f32 v[128:129], v[14:15], v[112:113]
	v_pk_fma_f32 v[126:127], v[16:17], v[22:23], v[126:127]
	v_pk_fma_f32 v[128:129], v[16:17], v[114:115], v[128:129]
	v_add_f32_e32 v124, v126, v127
	v_pk_fma_f32 v[14:15], v[28:29], v[120:121], v[14:15] op_sel_hi:[1,0,1]
	v_add_f32_e32 v131, v128, v129
	v_add_f32_dpp v124, v124, v124 quad_perm:[1,0,3,2] row_mask:0xf bank_mask:0xf bound_ctrl:1
	v_pk_fma_f32 v[16:17], v[30:31], v[120:121], v[16:17] op_sel_hi:[1,0,1]
	ds_read_b128 v[52:55], v18 offset:6656
	v_add_f32_dpp v124, v124, v124 quad_perm:[2,3,0,1] row_mask:0xf bank_mask:0xf bound_ctrl:1
	ds_read_b128 v[60:63], v18 offset:31232
	ds_read2_b32 v[122:123], v3 offset0:160 offset1:176
	v_add_f32_dpp v124, v124, v124 row_half_mirror row_mask:0xf bank_mask:0xf bound_ctrl:1
	ds_read_b128 v[56:59], v18 offset:14848
	ds_read_b128 v[64:67], v18 offset:39424
	v_add_f32_dpp v124, v124, v124 row_mirror row_mask:0xf bank_mask:0xf bound_ctrl:1
	v_pk_fma_f32 v[14:15], v[24:25], v[124:125], v[14:15] op_sel_hi:[1,0,1] neg_lo:[0,1,0] neg_hi:[0,1,0]
	v_pk_fma_f32 v[16:17], v[26:27], v[124:125], v[16:17] op_sel_hi:[1,0,1] neg_lo:[0,1,0] neg_hi:[0,1,0]
	v_add_f32_dpp v133, v130, v130 row_mirror row_mask:0xf bank_mask:0x3 bound_ctrl:1
	s_waitcnt lgkmcnt(6)
	v_pk_mul_f32 v[126:127], v[14:15], v[36:37]
	v_pk_mul_f32 v[128:129], v[14:15], v[32:33]
	v_pk_fma_f32 v[126:127], v[16:17], v[38:39], v[126:127]
	v_pk_fma_f32 v[128:129], v[16:17], v[34:35], v[128:129]
	v_add_f32_e32 v124, v126, v127
	v_pk_fma_f32 v[14:15], v[44:45], v[120:121], v[14:15] op_sel:[0,1,0]
	v_add_f32_e32 v130, v128, v129
	v_add_f32_dpp v124, v124, v124 quad_perm:[1,0,3,2] row_mask:0xf bank_mask:0xf bound_ctrl:1
	v_pk_fma_f32 v[16:17], v[46:47], v[120:121], v[16:17] op_sel:[0,1,0]
	ds_read_b128 v[100:103], v18 offset:6912
	v_add_f32_dpp v124, v124, v124 quad_perm:[2,3,0,1] row_mask:0xf bank_mask:0xf bound_ctrl:1
	ds_read_b128 v[108:111], v18 offset:31488
	ds_read_b128 v[116:119], v18 offset:23296
	v_add_f32_dpp v124, v124, v124 row_half_mirror row_mask:0xf bank_mask:0xf bound_ctrl:1
	ds_read_b128 v[104:107], v18 offset:15104
	ds_read_b128 v[112:115], v18 offset:39680
	v_add_f32_dpp v124, v124, v124 row_mirror row_mask:0xf bank_mask:0xf bound_ctrl:1
	v_pk_fma_f32 v[14:15], v[40:41], v[124:125], v[14:15] op_sel_hi:[1,0,1] neg_lo:[0,1,0] neg_hi:[0,1,0]
	v_pk_fma_f32 v[16:17], v[42:43], v[124:125], v[16:17] op_sel_hi:[1,0,1] neg_lo:[0,1,0] neg_hi:[0,1,0]
	v_add_f32_dpp v133, v131, v131 row_mirror row_mask:0xf bank_mask:0xc bound_ctrl:1
	v_add_f32_dpp v135, v132, v132 row_half_mirror row_mask:0xf bank_mask:0x5 bound_ctrl:1
	s_waitcnt lgkmcnt(6)
	v_pk_mul_f32 v[126:127], v[14:15], v[52:53]
	v_pk_mul_f32 v[128:129], v[14:15], v[48:49]
	v_pk_fma_f32 v[126:127], v[16:17], v[54:55], v[126:127]
	v_pk_fma_f32 v[128:129], v[16:17], v[50:51], v[128:129]
	v_add_f32_e32 v124, v126, v127
	v_pk_fma_f32 v[14:15], v[60:61], v[122:123], v[14:15] op_sel_hi:[1,0,1]
	v_add_f32_e32 v131, v128, v129
	v_add_f32_dpp v124, v124, v124 quad_perm:[1,0,3,2] row_mask:0xf bank_mask:0xf bound_ctrl:1
	v_pk_fma_f32 v[16:17], v[62:63], v[122:123], v[16:17] op_sel_hi:[1,0,1]
	ds_read_b128 v[20:23], v18 offset:7168
	v_add_f32_dpp v124, v124, v124 quad_perm:[2,3,0,1] row_mask:0xf bank_mask:0xf bound_ctrl:1
	ds_read_b128 v[28:31], v18 offset:31744
	ds_read2_b32 v[120:121], v3 offset0:192 offset1:208
	v_add_f32_dpp v124, v124, v124 row_half_mirror row_mask:0xf bank_mask:0xf bound_ctrl:1
	ds_read_b128 v[24:27], v18 offset:15360
	ds_read_b128 v[32:35], v18 offset:39936
	v_add_f32_dpp v124, v124, v124 row_mirror row_mask:0xf bank_mask:0xf bound_ctrl:1
	v_pk_fma_f32 v[14:15], v[56:57], v[124:125], v[14:15] op_sel_hi:[1,0,1] neg_lo:[0,1,0] neg_hi:[0,1,0]
	v_pk_fma_f32 v[16:17], v[58:59], v[124:125], v[16:17] op_sel_hi:[1,0,1] neg_lo:[0,1,0] neg_hi:[0,1,0]
	v_add_f32_dpp v135, v133, v133 row_half_mirror row_mask:0xf bank_mask:0xa bound_ctrl:1
	v_add_f32_dpp v138, v134, v134 quad_perm:[2,3,0,1] row_mask:0xf bank_mask:0xf bound_ctrl:1
	s_nop 0
	v_add_f32_dpp v98, v135, v135 quad_perm:[2,3,0,1] row_mask:0xf bank_mask:0xf bound_ctrl:1
	v_cndmask_b32_e64 v136, v138, v98, s[14:15]
	v_add_f32_dpp v132, v130, v130 row_mirror row_mask:0xf bank_mask:0x3 bound_ctrl:1
	s_waitcnt lgkmcnt(6)
	v_pk_mul_f32 v[126:127], v[14:15], v[100:101]
	v_pk_mul_f32 v[128:129], v[14:15], v[64:65]
	v_pk_fma_f32 v[126:127], v[16:17], v[102:103], v[126:127]
	v_pk_fma_f32 v[128:129], v[16:17], v[66:67], v[128:129]
	v_add_f32_e32 v124, v126, v127
	v_pk_fma_f32 v[14:15], v[108:109], v[122:123], v[14:15] op_sel:[0,1,0]
	v_add_f32_e32 v130, v128, v129
	v_add_f32_dpp v124, v124, v124 quad_perm:[1,0,3,2] row_mask:0xf bank_mask:0xf bound_ctrl:1
	v_pk_fma_f32 v[16:17], v[110:111], v[122:123], v[16:17] op_sel:[0,1,0]
	ds_read_b128 v[36:39], v18 offset:7424
	v_add_f32_dpp v124, v124, v124 quad_perm:[2,3,0,1] row_mask:0xf bank_mask:0xf bound_ctrl:1
	ds_read_b128 v[44:47], v18 offset:32000
	ds_read_b128 v[40:43], v18 offset:15616
	v_add_f32_dpp v124, v124, v124 row_half_mirror row_mask:0xf bank_mask:0xf bound_ctrl:1
	ds_read_b128 v[48:51], v18 offset:40192
	v_add_f32_dpp v132, v131, v131 row_mirror row_mask:0xf bank_mask:0xc bound_ctrl:1
	v_add_f32_dpp v124, v124, v124 row_mirror row_mask:0xf bank_mask:0xf bound_ctrl:1
	v_pk_fma_f32 v[14:15], v[104:105], v[124:125], v[14:15] op_sel_hi:[1,0,1] neg_lo:[0,1,0] neg_hi:[0,1,0]
	v_pk_fma_f32 v[16:17], v[106:107], v[124:125], v[16:17] op_sel_hi:[1,0,1] neg_lo:[0,1,0] neg_hi:[0,1,0]
	v_pk_mul_f32 v[14:15], v[14:15], v[116:117]
	v_pk_mul_f32 v[16:17], v[16:17], v[118:119]
	s_waitcnt lgkmcnt(5)
	v_pk_mul_f32 v[126:127], v[14:15], v[20:21]
	v_pk_mul_f32 v[128:129], v[14:15], v[112:113]
	v_pk_fma_f32 v[126:127], v[16:17], v[22:23], v[126:127]
	v_pk_fma_f32 v[128:129], v[16:17], v[114:115], v[128:129]
	v_add_f32_e32 v124, v126, v127
	v_pk_fma_f32 v[14:15], v[28:29], v[120:121], v[14:15] op_sel_hi:[1,0,1]
	v_add_f32_e32 v131, v128, v129
	v_add_f32_dpp v124, v124, v124 quad_perm:[1,0,3,2] row_mask:0xf bank_mask:0xf bound_ctrl:1
	v_pk_fma_f32 v[16:17], v[30:31], v[120:121], v[16:17] op_sel_hi:[1,0,1]
	ds_read_b128 v[52:55], v18 offset:7680
	v_add_f32_dpp v124, v124, v124 quad_perm:[2,3,0,1] row_mask:0xf bank_mask:0xf bound_ctrl:1
	ds_read_b128 v[60:63], v18 offset:32256
	ds_read2_b32 v[122:123], v3 offset0:224 offset1:240
	v_add_f32_dpp v124, v124, v124 row_half_mirror row_mask:0xf bank_mask:0xf bound_ctrl:1
	ds_read_b128 v[56:59], v18 offset:15872
	ds_read_b128 v[64:67], v18 offset:40448
	v_add_f32_dpp v124, v124, v124 row_mirror row_mask:0xf bank_mask:0xf bound_ctrl:1
	v_pk_fma_f32 v[14:15], v[24:25], v[124:125], v[14:15] op_sel_hi:[1,0,1] neg_lo:[0,1,0] neg_hi:[0,1,0]
	v_pk_fma_f32 v[16:17], v[26:27], v[124:125], v[16:17] op_sel_hi:[1,0,1] neg_lo:[0,1,0] neg_hi:[0,1,0]
	v_add_f32_dpp v133, v130, v130 row_mirror row_mask:0xf bank_mask:0x3 bound_ctrl:1
	s_waitcnt lgkmcnt(6)
	v_pk_mul_f32 v[126:127], v[14:15], v[36:37]
	v_pk_mul_f32 v[128:129], v[14:15], v[32:33]
	v_pk_fma_f32 v[126:127], v[16:17], v[38:39], v[126:127]
	v_pk_fma_f32 v[128:129], v[16:17], v[34:35], v[128:129]
	v_add_f32_e32 v124, v126, v127
	v_pk_fma_f32 v[14:15], v[44:45], v[120:121], v[14:15] op_sel:[0,1,0]
	v_add_f32_e32 v130, v128, v129
	v_add_f32_dpp v124, v124, v124 quad_perm:[1,0,3,2] row_mask:0xf bank_mask:0xf bound_ctrl:1
	v_pk_fma_f32 v[16:17], v[46:47], v[120:121], v[16:17] op_sel:[0,1,0]
	ds_read_b128 v[100:103], v18 offset:7936
	v_add_f32_dpp v124, v124, v124 quad_perm:[2,3,0,1] row_mask:0xf bank_mask:0xf bound_ctrl:1
	ds_read_b128 v[108:111], v18 offset:32512
	ds_read_b128 v[116:119], v18 offset:24320
	v_add_f32_dpp v124, v124, v124 row_half_mirror row_mask:0xf bank_mask:0xf bound_ctrl:1
	ds_read_b128 v[104:107], v18 offset:16128
	ds_read_b128 v[112:115], v18 offset:40704
	v_add_f32_dpp v124, v124, v124 row_mirror row_mask:0xf bank_mask:0xf bound_ctrl:1
	v_pk_fma_f32 v[14:15], v[40:41], v[124:125], v[14:15] op_sel_hi:[1,0,1] neg_lo:[0,1,0] neg_hi:[0,1,0]
	v_pk_fma_f32 v[16:17], v[42:43], v[124:125], v[16:17] op_sel_hi:[1,0,1] neg_lo:[0,1,0] neg_hi:[0,1,0]
	v_add_f32_dpp v133, v131, v131 row_mirror row_mask:0xf bank_mask:0xc bound_ctrl:1
	v_add_f32_dpp v134, v132, v132 row_half_mirror row_mask:0xf bank_mask:0x5 bound_ctrl:1
	s_waitcnt lgkmcnt(6)
	v_pk_mul_f32 v[126:127], v[14:15], v[52:53]
	v_pk_mul_f32 v[128:129], v[14:15], v[48:49]
	v_pk_fma_f32 v[126:127], v[16:17], v[54:55], v[126:127]
	v_pk_fma_f32 v[128:129], v[16:17], v[50:51], v[128:129]
	v_add_f32_e32 v124, v126, v127
	v_pk_fma_f32 v[14:15], v[60:61], v[122:123], v[14:15] op_sel_hi:[1,0,1]
	v_add_f32_e32 v131, v128, v129
	v_add_f32_dpp v124, v124, v124 quad_perm:[1,0,3,2] row_mask:0xf bank_mask:0xf bound_ctrl:1
	v_pk_fma_f32 v[16:17], v[62:63], v[122:123], v[16:17] op_sel_hi:[1,0,1]
	ds_read_b128 v[20:23], v68
	v_add_f32_dpp v124, v124, v124 quad_perm:[2,3,0,1] row_mask:0xf bank_mask:0xf bound_ctrl:1
	ds_read_b128 v[28:31], v68 offset:24576
	ds_read2_b32 v[120:121], v69 offset1:16
	v_add_f32_dpp v124, v124, v124 row_half_mirror row_mask:0xf bank_mask:0xf bound_ctrl:1
	ds_read_b128 v[24:27], v68 offset:8192
	ds_read_b128 v[32:35], v68 offset:32768
	v_add_f32_dpp v124, v124, v124 row_mirror row_mask:0xf bank_mask:0xf bound_ctrl:1
	v_pk_fma_f32 v[14:15], v[56:57], v[124:125], v[14:15] op_sel_hi:[1,0,1] neg_lo:[0,1,0] neg_hi:[0,1,0]
	v_pk_fma_f32 v[16:17], v[58:59], v[124:125], v[16:17] op_sel_hi:[1,0,1] neg_lo:[0,1,0] neg_hi:[0,1,0]
	v_add_f32_dpp v134, v133, v133 row_half_mirror row_mask:0xf bank_mask:0xa bound_ctrl:1
	v_add_f32_dpp v132, v130, v130 row_mirror row_mask:0xf bank_mask:0x3 bound_ctrl:1
	s_waitcnt lgkmcnt(6)
	v_pk_mul_f32 v[126:127], v[14:15], v[100:101]
	v_pk_mul_f32 v[128:129], v[14:15], v[64:65]
	v_pk_fma_f32 v[126:127], v[16:17], v[102:103], v[126:127]
	v_pk_fma_f32 v[128:129], v[16:17], v[66:67], v[128:129]
	v_add_f32_e32 v124, v126, v127
	v_pk_fma_f32 v[14:15], v[108:109], v[122:123], v[14:15] op_sel:[0,1,0]
	v_add_f32_e32 v130, v128, v129
	v_add_f32_dpp v124, v124, v124 quad_perm:[1,0,3,2] row_mask:0xf bank_mask:0xf bound_ctrl:1
	v_pk_fma_f32 v[16:17], v[110:111], v[122:123], v[16:17] op_sel:[0,1,0]
	ds_read_b128 v[36:39], v68 offset:256
	v_add_f32_dpp v124, v124, v124 quad_perm:[2,3,0,1] row_mask:0xf bank_mask:0xf bound_ctrl:1
	ds_read_b128 v[44:47], v68 offset:24832
	ds_read_b128 v[40:43], v68 offset:8448
	v_add_f32_dpp v124, v124, v124 row_half_mirror row_mask:0xf bank_mask:0xf bound_ctrl:1
	ds_read_b128 v[48:51], v68 offset:33024
	v_add_f32_dpp v132, v131, v131 row_mirror row_mask:0xf bank_mask:0xc bound_ctrl:1
	v_add_f32_dpp v124, v124, v124 row_mirror row_mask:0xf bank_mask:0xf bound_ctrl:1
	v_pk_fma_f32 v[14:15], v[104:105], v[124:125], v[14:15] op_sel_hi:[1,0,1] neg_lo:[0,1,0] neg_hi:[0,1,0]
	v_pk_fma_f32 v[16:17], v[106:107], v[124:125], v[16:17] op_sel_hi:[1,0,1] neg_lo:[0,1,0] neg_hi:[0,1,0]
	v_pk_mul_f32 v[14:15], v[14:15], v[116:117]
	v_pk_mul_f32 v[16:17], v[16:17], v[118:119]
	s_add_i32 s8, s8, 1
	s_add_i32 s71, s71, 32
	s_cmpk_lg_i32 s8, 0x88
	s_barrier
	s_cbranch_scc0 .LBB0_618

.LBB0_618:
	s_waitcnt lgkmcnt(0)
	s_waitcnt lgkmcnt(9)
	v_pk_mul_f32 v[128:129], v[14:15], v[112:113]
	s_nop 0
	v_pk_fma_f32 v[128:129], v[16:17], v[114:115], v[128:129]
	s_nop 0
	v_add_f32_e32 v131, v128, v129
	v_add_f32_dpp v133, v130, v130 row_mirror row_mask:0xf bank_mask:0x3 bound_ctrl:1
	s_nop 0
	v_add_f32_dpp v133, v131, v131 row_mirror row_mask:0xf bank_mask:0xc bound_ctrl:1
	v_add_f32_dpp v135, v132, v132 row_half_mirror row_mask:0xf bank_mask:0x5 bound_ctrl:1
	s_nop 0
	v_add_f32_dpp v135, v133, v133 row_half_mirror row_mask:0xf bank_mask:0xa bound_ctrl:1
	v_add_f32_dpp v138, v134, v134 quad_perm:[2,3,0,1] row_mask:0xf bank_mask:0xf bound_ctrl:1
	s_nop 0
	v_add_f32_dpp v98, v135, v135 quad_perm:[2,3,0,1] row_mask:0xf bank_mask:0xf bound_ctrl:1
	v_cndmask_b32_e64 v137, v138, v98, s[14:15]
	v_add_f32_dpp v138, v136, v136 quad_perm:[1,0,3,2] row_mask:0xf bank_mask:0xf bound_ctrl:1
	s_nop 0
	v_add_f32_dpp v98, v137, v137 quad_perm:[1,0,3,2] row_mask:0xf bank_mask:0xf bound_ctrl:1
	v_cndmask_b32_e64 v99, v138, v98, s[16:17]
	v_bfe_u32 v7, v99, 16, 1
	v_add3_u32 v7, v99, v7, s3
	global_store_short_d16_hi v[8:9], v7, off
	s_branch .LBB0_603

.Lld_ldone_p1:
	s_waitcnt vmcnt(21)
	s_mov_b32 s88, 0
	v_add_u32_e32 v83, s88, v7
	v_add_u32_e32 v96, s88, v8
	v_lshlrev_b32_e32 v92, 16, v29
	v_and_b32_e32 v93, s89, v29
	ds_write_b64 v96, v[92:93]
	v_lshlrev_b32_e32 v92, 16, v9
	v_and_b32_e32 v93, s89, v9
	v_mul_f32_e32 v84, 0x3fb8aa3b, v92
	v_mul_f32_e32 v85, 0x3fb8aa3b, v93
	v_lshlrev_b32_e32 v94, 16, v13
	v_and_b32_e32 v95, s89, v13
	ds_write_b64 v83, v[94:95] offset:0
	v_exp_f32_e64 v86, -v84
	v_exp_f32_e64 v87, -v85
	v_exp_f32_e32 v90, v84
	v_exp_f32_e32 v91, v85
	v_lshlrev_b32_e32 v92, 16, v17
	v_and_b32_e32 v93, s89, v17
	v_mul_f32_e32 v92, v92, v90
	v_mul_f32_e32 v93, v93, v91
	ds_write_b64 v83, v[92:93] offset:8192
	ds_write_b64 v83, v[86:87] offset:16384
	v_lshlrev_b32_e32 v94, 16, v21
	v_and_b32_e32 v95, s89, v21
	v_mul_f32_e32 v94, v94, v90
	v_mul_f32_e32 v95, v95, v91
	ds_write_b64 v83, v[94:95] offset:24576
	v_lshlrev_b32_e32 v92, 16, v25
	v_and_b32_e32 v93, s89, v25
	v_mul_f32_e32 v92, v92, v86
	v_mul_f32_e32 v93, v93, v87
	ds_write_b64 v83, v[92:93] offset:32768
	v_lshlrev_b32_e32 v92, 16, v10
	v_and_b32_e32 v93, s89, v10
	v_fmac_f32_e32 v84, 0x3fb8aa3b, v92
	v_fmac_f32_e32 v85, 0x3fb8aa3b, v93
	v_lshlrev_b32_e32 v94, 16, v14
	v_and_b32_e32 v95, s89, v14
	v_mul_f32_e32 v94, v94, v86
	v_mul_f32_e32 v95, v95, v87
	ds_write_b64 v83, v[94:95] offset:256
	v_exp_f32_e64 v88, -v84
	v_exp_f32_e64 v89, -v85
	v_exp_f32_e32 v90, v84
	v_exp_f32_e32 v91, v85
	v_lshlrev_b32_e32 v92, 16, v18
	v_and_b32_e32 v93, s89, v18
	v_mul_f32_e32 v92, v92, v90
	v_mul_f32_e32 v93, v93, v91
	ds_write_b64 v83, v[92:93] offset:8448
	ds_write_b64 v83, v[88:89] offset:16640
	v_lshlrev_b32_e32 v94, 16, v22
	v_and_b32_e32 v95, s89, v22
	v_mul_f32_e32 v94, v94, v90
	v_mul_f32_e32 v95, v95, v91
	ds_write_b64 v83, v[94:95] offset:24832
	v_lshlrev_b32_e32 v92, 16, v26
	v_and_b32_e32 v93, s89, v26
	v_mul_f32_e32 v92, v92, v88
	v_mul_f32_e32 v93, v93, v89
	ds_write_b64 v83, v[92:93] offset:33024
	v_lshlrev_b32_e32 v92, 16, v11
	v_and_b32_e32 v93, s89, v11
	v_fmac_f32_e32 v84, 0x3fb8aa3b, v92
	v_fmac_f32_e32 v85, 0x3fb8aa3b, v93
	v_lshlrev_b32_e32 v94, 16, v15
	v_and_b32_e32 v95, s89, v15
	v_mul_f32_e32 v94, v94, v88
	v_mul_f32_e32 v95, v95, v89
	ds_write_b64 v83, v[94:95] offset:512
	v_exp_f32_e64 v86, -v84
	v_exp_f32_e64 v87, -v85
	v_exp_f32_e32 v90, v84
	v_exp_f32_e32 v91, v85
	v_lshlrev_b32_e32 v92, 16, v19
	v_and_b32_e32 v93, s89, v19
	v_mul_f32_e32 v92, v92, v90
	v_mul_f32_e32 v93, v93, v91
	ds_write_b64 v83, v[92:93] offset:8704
	ds_write_b64 v83, v[86:87] offset:16896
	v_lshlrev_b32_e32 v94, 16, v23
	v_and_b32_e32 v95, s89, v23
	v_mul_f32_e32 v94, v94, v90
	v_mul_f32_e32 v95, v95, v91
	ds_write_b64 v83, v[94:95] offset:25088
	v_lshlrev_b32_e32 v92, 16, v27
	v_and_b32_e32 v93, s89, v27
	v_mul_f32_e32 v92, v92, v86
	v_mul_f32_e32 v93, v93, v87
	ds_write_b64 v83, v[92:93] offset:33280
	v_lshlrev_b32_e32 v92, 16, v12
	v_and_b32_e32 v93, s89, v12
	v_fmac_f32_e32 v84, 0x3fb8aa3b, v92
	v_fmac_f32_e32 v85, 0x3fb8aa3b, v93
	v_lshlrev_b32_e32 v94, 16, v16
	v_and_b32_e32 v95, s89, v16
	v_mul_f32_e32 v94, v94, v86
	v_mul_f32_e32 v95, v95, v87
	ds_write_b64 v83, v[94:95] offset:768
	v_exp_f32_e64 v88, -v84
	v_exp_f32_e64 v89, -v85
	v_exp_f32_e32 v90, v84
	v_exp_f32_e32 v91, v85
	v_lshlrev_b32_e32 v92, 16, v20
	v_and_b32_e32 v93, s89, v20
	v_mul_f32_e32 v92, v92, v90
	v_mul_f32_e32 v93, v93, v91
	ds_write_b64 v83, v[92:93] offset:8960
	ds_write_b64 v83, v[88:89] offset:17152
	v_lshlrev_b32_e32 v94, 16, v24
	v_and_b32_e32 v95, s89, v24
	v_mul_f32_e32 v94, v94, v90
	v_mul_f32_e32 v95, v95, v91
	ds_write_b64 v83, v[94:95] offset:25344
	v_lshlrev_b32_e32 v92, 16, v28
	v_and_b32_e32 v93, s89, v28
	ds_write_b64 v83, v[92:93] offset:33536
	s_mov_b32 s8, 2
	s_lshl_b32 s9, s8, 5
	s_lshl_b32 s33, s81, 3
	s_add_i32 s9, s9, s33
	s_lshl_b32 s33, s6, 8
	s_add_i32 s33, s33, 0x8000
	s_lshl_b32 s45, s6, 12
	s_cmp_lt_u32 s8, 8
	s_cselect_b32 s33, s33, s45
	s_cselect_b32 s44, 0, 0x100
	s_movk_i32 s45, 0xff8
	s_cselect_b32 s45, 0xf8, s45
	s_sub_i32 s9, s9, s44
	s_sub_i32 s45, s45, s9
	s_cmp_lg_u32 s50, 0
	s_cselect_b32 s9, s45, s9
	s_add_i32 s33, s33, s9
	s_lshl_b32 s33, s33, 9
	s_cmp_lg_u32 s50, 0
	s_cbranch_scc1 .Lld_bw_p2
	s_add_u32 s0, s82, s33
	s_addc_u32 s1, s83, 0
	global_load_dword v9, v3, s[0:1]
	global_load_dword v10, v3, s[0:1] offset:512
	global_load_dword v11, v3, s[0:1] offset:1024
	global_load_dword v12, v3, s[0:1] offset:1536
	s_add_u32 s0, s62, s33
	s_addc_u32 s1, s63, 0
	global_load_dword v13, v3, s[0:1]
	global_load_dword v14, v3, s[0:1] offset:512
	global_load_dword v15, v3, s[0:1] offset:1024
	global_load_dword v16, v3, s[0:1] offset:1536
	s_add_u32 s0, s70, s33
	s_addc_u32 s1, s71, 0
	global_load_dword v17, v3, s[0:1]
	global_load_dword v18, v3, s[0:1] offset:512
	global_load_dword v19, v3, s[0:1] offset:1024
	global_load_dword v20, v3, s[0:1] offset:1536
	s_add_u32 s0, s72, s33
	s_addc_u32 s1, s73, 0
	global_load_dword v21, v3, s[0:1]
	global_load_dword v22, v3, s[0:1] offset:512
	global_load_dword v23, v3, s[0:1] offset:1024
	global_load_dword v24, v3, s[0:1] offset:1536
	s_add_u32 s0, s74, s33
	s_addc_u32 s1, s75, 0
	global_load_dword v25, v3, s[0:1]
	global_load_dword v26, v3, s[0:1] offset:512
	global_load_dword v27, v3, s[0:1] offset:1024
	global_load_dword v28, v3, s[0:1] offset:1536
	s_add_u32 s0, s84, s33
	s_addc_u32 s1, s85, 0
	global_load_dword v29, v6, s[0:1]
	s_branch .Lld_ldone_p2

.Lld_ldone_p2:
	s_waitcnt vmcnt(21)
	s_mov_b32 s88, 0xa800
	v_add_u32_e32 v83, s88, v7
	v_add_u32_e32 v96, s88, v8
	v_lshlrev_b32_e32 v92, 16, v118
	v_and_b32_e32 v93, s89, v118
	ds_write_b64 v96, v[92:93]
	v_lshlrev_b32_e32 v92, 16, v98
	v_and_b32_e32 v93, s89, v98
	v_mul_f32_e32 v84, 0x3fb8aa3b, v92
	v_mul_f32_e32 v85, 0x3fb8aa3b, v93
	v_lshlrev_b32_e32 v94, 16, v102
	v_and_b32_e32 v95, s89, v102
	ds_write_b64 v83, v[94:95] offset:0
	v_exp_f32_e64 v86, -v84
	v_exp_f32_e64 v87, -v85
	v_exp_f32_e32 v90, v84
	v_exp_f32_e32 v91, v85
	v_lshlrev_b32_e32 v92, 16, v106
	v_and_b32_e32 v93, s89, v106
	v_mul_f32_e32 v92, v92, v90
	v_mul_f32_e32 v93, v93, v91
	ds_write_b64 v83, v[92:93] offset:8192
	ds_write_b64 v83, v[86:87] offset:16384
	v_lshlrev_b32_e32 v94, 16, v110
	v_and_b32_e32 v95, s89, v110
	v_mul_f32_e32 v94, v94, v90
	v_mul_f32_e32 v95, v95, v91
	ds_write_b64 v83, v[94:95] offset:24576
	v_lshlrev_b32_e32 v92, 16, v114
	v_and_b32_e32 v93, s89, v114
	v_mul_f32_e32 v92, v92, v86
	v_mul_f32_e32 v93, v93, v87
	ds_write_b64 v83, v[92:93] offset:32768
	v_lshlrev_b32_e32 v92, 16, v99
	v_and_b32_e32 v93, s89, v99
	v_fmac_f32_e32 v84, 0x3fb8aa3b, v92
	v_fmac_f32_e32 v85, 0x3fb8aa3b, v93
	v_lshlrev_b32_e32 v94, 16, v103
	v_and_b32_e32 v95, s89, v103
	v_mul_f32_e32 v94, v94, v86
	v_mul_f32_e32 v95, v95, v87
	ds_write_b64 v83, v[94:95] offset:256
	v_exp_f32_e64 v88, -v84
	v_exp_f32_e64 v89, -v85
	v_exp_f32_e32 v90, v84
	v_exp_f32_e32 v91, v85
	v_lshlrev_b32_e32 v92, 16, v107
	v_and_b32_e32 v93, s89, v107
	v_mul_f32_e32 v92, v92, v90
	v_mul_f32_e32 v93, v93, v91
	ds_write_b64 v83, v[92:93] offset:8448
	ds_write_b64 v83, v[88:89] offset:16640
	v_lshlrev_b32_e32 v94, 16, v111
	v_and_b32_e32 v95, s89, v111
	v_mul_f32_e32 v94, v94, v90
	v_mul_f32_e32 v95, v95, v91
	ds_write_b64 v83, v[94:95] offset:24832
	v_lshlrev_b32_e32 v92, 16, v115
	v_and_b32_e32 v93, s89, v115
	v_mul_f32_e32 v92, v92, v88
	v_mul_f32_e32 v93, v93, v89
	ds_write_b64 v83, v[92:93] offset:33024
	v_lshlrev_b32_e32 v92, 16, v100
	v_and_b32_e32 v93, s89, v100
	v_fmac_f32_e32 v84, 0x3fb8aa3b, v92
	v_fmac_f32_e32 v85, 0x3fb8aa3b, v93
	v_lshlrev_b32_e32 v94, 16, v104
	v_and_b32_e32 v95, s89, v104
	v_mul_f32_e32 v94, v94, v88
	v_mul_f32_e32 v95, v95, v89
	ds_write_b64 v83, v[94:95] offset:512
	v_exp_f32_e64 v86, -v84
	v_exp_f32_e64 v87, -v85
	v_exp_f32_e32 v90, v84
	v_exp_f32_e32 v91, v85
	v_lshlrev_b32_e32 v92, 16, v108
	v_and_b32_e32 v93, s89, v108
	v_mul_f32_e32 v92, v92, v90
	v_mul_f32_e32 v93, v93, v91
	ds_write_b64 v83, v[92:93] offset:8704
	ds_write_b64 v83, v[86:87] offset:16896
	v_lshlrev_b32_e32 v94, 16, v112
	v_and_b32_e32 v95, s89, v112
	v_mul_f32_e32 v94, v94, v90
	v_mul_f32_e32 v95, v95, v91
	ds_write_b64 v83, v[94:95] offset:25088
	v_lshlrev_b32_e32 v92, 16, v116
	v_and_b32_e32 v93, s89, v116
	v_mul_f32_e32 v92, v92, v86
	v_mul_f32_e32 v93, v93, v87
	ds_write_b64 v83, v[92:93] offset:33280
	v_lshlrev_b32_e32 v92, 16, v101
	v_and_b32_e32 v93, s89, v101
	v_fmac_f32_e32 v84, 0x3fb8aa3b, v92
	v_fmac_f32_e32 v85, 0x3fb8aa3b, v93
	v_lshlrev_b32_e32 v94, 16, v105
	v_and_b32_e32 v95, s89, v105
	v_mul_f32_e32 v94, v94, v86
	v_mul_f32_e32 v95, v95, v87
	ds_write_b64 v83, v[94:95] offset:768
	v_exp_f32_e64 v88, -v84
	v_exp_f32_e64 v89, -v85
	v_exp_f32_e32 v90, v84
	v_exp_f32_e32 v91, v85
	v_lshlrev_b32_e32 v92, 16, v109
	v_and_b32_e32 v93, s89, v109
	v_mul_f32_e32 v92, v92, v90
	v_mul_f32_e32 v93, v93, v91
	ds_write_b64 v83, v[92:93] offset:8960
	ds_write_b64 v83, v[88:89] offset:17152
	v_lshlrev_b32_e32 v94, 16, v113
	v_and_b32_e32 v95, s89, v113
	v_mul_f32_e32 v94, v94, v90
	v_mul_f32_e32 v95, v95, v91
	ds_write_b64 v83, v[94:95] offset:25344
	v_lshlrev_b32_e32 v92, 16, v117
	v_and_b32_e32 v93, s89, v117
	ds_write_b64 v83, v[92:93] offset:33536
	s_mov_b32 s88, 0x15000
	s_mov_b32 s86, 0
	s_waitcnt lgkmcnt(0)
	s_barrier

.Lld_nocvt_a:
	s_add_i32 s8, s86, 3
	s_cmp_lt_u32 s8, 0x88
	s_cbranch_scc0 .Lld_noload_a
	s_lshl_b32 s9, s8, 5
	s_lshl_b32 s33, s81, 3
	s_add_i32 s9, s9, s33
	s_lshl_b32 s33, s6, 8
	s_add_i32 s33, s33, 0x8000
	s_lshl_b32 s45, s6, 12
	s_cmp_lt_u32 s8, 8
	s_cselect_b32 s33, s33, s45
	s_cselect_b32 s44, 0, 0x100
	s_movk_i32 s45, 0xff8
	s_cselect_b32 s45, 0xf8, s45
	s_sub_i32 s9, s9, s44
	s_sub_i32 s45, s45, s9
	s_cmp_lg_u32 s50, 0
	s_cselect_b32 s9, s45, s9
	s_add_i32 s33, s33, s9
	s_lshl_b32 s33, s33, 9
	s_cmp_lg_u32 s50, 0
	s_cbranch_scc1 .Lld_bw_a
	s_add_u32 s0, s82, s33
	s_addc_u32 s1, s83, 0
	global_load_dword v98, v3, s[0:1]
	global_load_dword v99, v3, s[0:1] offset:512
	global_load_dword v100, v3, s[0:1] offset:1024
	global_load_dword v101, v3, s[0:1] offset:1536
	s_add_u32 s0, s62, s33
	s_addc_u32 s1, s63, 0
	global_load_dword v102, v3, s[0:1]
	global_load_dword v103, v3, s[0:1] offset:512
	global_load_dword v104, v3, s[0:1] offset:1024
	global_load_dword v105, v3, s[0:1] offset:1536
	s_add_u32 s0, s70, s33
	s_addc_u32 s1, s71, 0
	global_load_dword v106, v3, s[0:1]
	global_load_dword v107, v3, s[0:1] offset:512
	global_load_dword v108, v3, s[0:1] offset:1024
	global_load_dword v109, v3, s[0:1] offset:1536
	s_add_u32 s0, s72, s33
	s_addc_u32 s1, s73, 0
	global_load_dword v110, v3, s[0:1]
	global_load_dword v111, v3, s[0:1] offset:512
	global_load_dword v112, v3, s[0:1] offset:1024
	global_load_dword v113, v3, s[0:1] offset:1536
	s_add_u32 s0, s74, s33
	s_addc_u32 s1, s75, 0
	global_load_dword v114, v3, s[0:1]
	global_load_dword v115, v3, s[0:1] offset:512
	global_load_dword v116, v3, s[0:1] offset:1024
	global_load_dword v117, v3, s[0:1] offset:1536
	s_add_u32 s0, s84, s33
	s_addc_u32 s1, s85, 0
	global_load_dword v118, v6, s[0:1]
	s_branch .Lld_ldone_a

.Lld_proc_a:
	s_add_i32 s8, s86, 2
	s_cmp_lt_u32 s8, 0x88
	s_cbranch_scc0 .Lld_noproc_a
	v_add_u32_e32 v83, s88, v7
	v_add_u32_e32 v96, s88, v8
	v_lshlrev_b32_e32 v92, 16, v29
	v_and_b32_e32 v93, s89, v29
	ds_write_b64 v96, v[92:93]
	v_lshlrev_b32_e32 v92, 16, v9
	v_and_b32_e32 v93, s89, v9
	v_mul_f32_e32 v84, 0x3fb8aa3b, v92
	v_mul_f32_e32 v85, 0x3fb8aa3b, v93
	v_lshlrev_b32_e32 v94, 16, v13
	v_and_b32_e32 v95, s89, v13
	ds_write_b64 v83, v[94:95] offset:0
	v_exp_f32_e64 v86, -v84
	v_exp_f32_e64 v87, -v85
	v_exp_f32_e32 v90, v84
	v_exp_f32_e32 v91, v85
	v_lshlrev_b32_e32 v92, 16, v17
	v_and_b32_e32 v93, s89, v17
	v_mul_f32_e32 v92, v92, v90
	v_mul_f32_e32 v93, v93, v91
	ds_write_b64 v83, v[92:93] offset:8192
	ds_write_b64 v83, v[86:87] offset:16384
	v_lshlrev_b32_e32 v94, 16, v21
	v_and_b32_e32 v95, s89, v21
	v_mul_f32_e32 v94, v94, v90
	v_mul_f32_e32 v95, v95, v91
	ds_write_b64 v83, v[94:95] offset:24576
	v_lshlrev_b32_e32 v92, 16, v25
	v_and_b32_e32 v93, s89, v25
	v_mul_f32_e32 v92, v92, v86
	v_mul_f32_e32 v93, v93, v87
	ds_write_b64 v83, v[92:93] offset:32768
	v_lshlrev_b32_e32 v92, 16, v10
	v_and_b32_e32 v93, s89, v10
	v_fmac_f32_e32 v84, 0x3fb8aa3b, v92
	v_fmac_f32_e32 v85, 0x3fb8aa3b, v93
	v_lshlrev_b32_e32 v94, 16, v14
	v_and_b32_e32 v95, s89, v14
	v_mul_f32_e32 v94, v94, v86
	v_mul_f32_e32 v95, v95, v87
	ds_write_b64 v83, v[94:95] offset:256
	v_exp_f32_e64 v88, -v84
	v_exp_f32_e64 v89, -v85
	v_exp_f32_e32 v90, v84
	v_exp_f32_e32 v91, v85
	v_lshlrev_b32_e32 v92, 16, v18
	v_and_b32_e32 v93, s89, v18
	v_mul_f32_e32 v92, v92, v90
	v_mul_f32_e32 v93, v93, v91
	ds_write_b64 v83, v[92:93] offset:8448
	ds_write_b64 v83, v[88:89] offset:16640
	v_lshlrev_b32_e32 v94, 16, v22
	v_and_b32_e32 v95, s89, v22
	v_mul_f32_e32 v94, v94, v90
	v_mul_f32_e32 v95, v95, v91
	ds_write_b64 v83, v[94:95] offset:24832
	v_lshlrev_b32_e32 v92, 16, v26
	v_and_b32_e32 v93, s89, v26
	v_mul_f32_e32 v92, v92, v88
	v_mul_f32_e32 v93, v93, v89
	ds_write_b64 v83, v[92:93] offset:33024
	v_lshlrev_b32_e32 v92, 16, v11
	v_and_b32_e32 v93, s89, v11
	v_fmac_f32_e32 v84, 0x3fb8aa3b, v92
	v_fmac_f32_e32 v85, 0x3fb8aa3b, v93
	v_lshlrev_b32_e32 v94, 16, v15
	v_and_b32_e32 v95, s89, v15
	v_mul_f32_e32 v94, v94, v88
	v_mul_f32_e32 v95, v95, v89
	ds_write_b64 v83, v[94:95] offset:512
	v_exp_f32_e64 v86, -v84
	v_exp_f32_e64 v87, -v85
	v_exp_f32_e32 v90, v84
	v_exp_f32_e32 v91, v85
	v_lshlrev_b32_e32 v92, 16, v19
	v_and_b32_e32 v93, s89, v19
	v_mul_f32_e32 v92, v92, v90
	v_mul_f32_e32 v93, v93, v91
	ds_write_b64 v83, v[92:93] offset:8704
	ds_write_b64 v83, v[86:87] offset:16896
	v_lshlrev_b32_e32 v94, 16, v23
	v_and_b32_e32 v95, s89, v23
	v_mul_f32_e32 v94, v94, v90
	v_mul_f32_e32 v95, v95, v91
	ds_write_b64 v83, v[94:95] offset:25088
	v_lshlrev_b32_e32 v92, 16, v27
	v_and_b32_e32 v93, s89, v27
	v_mul_f32_e32 v92, v92, v86
	v_mul_f32_e32 v93, v93, v87
	ds_write_b64 v83, v[92:93] offset:33280
	v_lshlrev_b32_e32 v92, 16, v12
	v_and_b32_e32 v93, s89, v12
	v_fmac_f32_e32 v84, 0x3fb8aa3b, v92
	v_fmac_f32_e32 v85, 0x3fb8aa3b, v93
	v_lshlrev_b32_e32 v94, 16, v16
	v_and_b32_e32 v95, s89, v16
	v_mul_f32_e32 v94, v94, v86
	v_mul_f32_e32 v95, v95, v87
	ds_write_b64 v83, v[94:95] offset:768
	v_exp_f32_e64 v88, -v84
	v_exp_f32_e64 v89, -v85
	v_exp_f32_e32 v90, v84
	v_exp_f32_e32 v91, v85
	v_lshlrev_b32_e32 v92, 16, v20
	v_and_b32_e32 v93, s89, v20
	v_mul_f32_e32 v92, v92, v90
	v_mul_f32_e32 v93, v93, v91
	ds_write_b64 v83, v[92:93] offset:8960
	ds_write_b64 v83, v[88:89] offset:17152
	v_lshlrev_b32_e32 v94, 16, v24
	v_and_b32_e32 v95, s89, v24
	v_mul_f32_e32 v94, v94, v90
	v_mul_f32_e32 v95, v95, v91
	ds_write_b64 v83, v[94:95] offset:25344
	v_lshlrev_b32_e32 v92, 16, v28
	v_and_b32_e32 v93, s89, v28
	ds_write_b64 v83, v[92:93] offset:33536

.Lld_nocvt_b:
	s_add_i32 s8, s86, 3
	s_cmp_lt_u32 s8, 0x88
	s_cbranch_scc0 .Lld_noload_b
	s_lshl_b32 s9, s8, 5
	s_lshl_b32 s33, s81, 3
	s_add_i32 s9, s9, s33
	s_lshl_b32 s33, s6, 8
	s_add_i32 s33, s33, 0x8000
	s_lshl_b32 s45, s6, 12
	s_cmp_lt_u32 s8, 8
	s_cselect_b32 s33, s33, s45
	s_cselect_b32 s44, 0, 0x100
	s_movk_i32 s45, 0xff8
	s_cselect_b32 s45, 0xf8, s45
	s_sub_i32 s9, s9, s44
	s_sub_i32 s45, s45, s9
	s_cmp_lg_u32 s50, 0
	s_cselect_b32 s9, s45, s9
	s_add_i32 s33, s33, s9
	s_lshl_b32 s33, s33, 9
	s_cmp_lg_u32 s50, 0
	s_cbranch_scc1 .Lld_bw_b
	s_add_u32 s0, s82, s33
	s_addc_u32 s1, s83, 0
	global_load_dword v9, v3, s[0:1]
	global_load_dword v10, v3, s[0:1] offset:512
	global_load_dword v11, v3, s[0:1] offset:1024
	global_load_dword v12, v3, s[0:1] offset:1536
	s_add_u32 s0, s62, s33
	s_addc_u32 s1, s63, 0
	global_load_dword v13, v3, s[0:1]
	global_load_dword v14, v3, s[0:1] offset:512
	global_load_dword v15, v3, s[0:1] offset:1024
	global_load_dword v16, v3, s[0:1] offset:1536
	s_add_u32 s0, s70, s33
	s_addc_u32 s1, s71, 0
	global_load_dword v17, v3, s[0:1]
	global_load_dword v18, v3, s[0:1] offset:512
	global_load_dword v19, v3, s[0:1] offset:1024
	global_load_dword v20, v3, s[0:1] offset:1536
	s_add_u32 s0, s72, s33
	s_addc_u32 s1, s73, 0
	global_load_dword v21, v3, s[0:1]
	global_load_dword v22, v3, s[0:1] offset:512
	global_load_dword v23, v3, s[0:1] offset:1024
	global_load_dword v24, v3, s[0:1] offset:1536
	s_add_u32 s0, s74, s33
	s_addc_u32 s1, s75, 0
	global_load_dword v25, v3, s[0:1]
	global_load_dword v26, v3, s[0:1] offset:512
	global_load_dword v27, v3, s[0:1] offset:1024
	global_load_dword v28, v3, s[0:1] offset:1536
	s_add_u32 s0, s84, s33
	s_addc_u32 s1, s85, 0
	global_load_dword v29, v6, s[0:1]
	s_branch .Lld_ldone_b

.Lld_proc_b:
	s_add_i32 s8, s86, 2
	s_cmp_lt_u32 s8, 0x88
	s_cbranch_scc0 .Lld_noproc_b
	v_add_u32_e32 v83, s88, v7
	v_add_u32_e32 v96, s88, v8
	v_lshlrev_b32_e32 v92, 16, v118
	v_and_b32_e32 v93, s89, v118
	ds_write_b64 v96, v[92:93]
	v_lshlrev_b32_e32 v92, 16, v98
	v_and_b32_e32 v93, s89, v98
	v_mul_f32_e32 v84, 0x3fb8aa3b, v92
	v_mul_f32_e32 v85, 0x3fb8aa3b, v93
	v_lshlrev_b32_e32 v94, 16, v102
	v_and_b32_e32 v95, s89, v102
	ds_write_b64 v83, v[94:95] offset:0
	v_exp_f32_e64 v86, -v84
	v_exp_f32_e64 v87, -v85
	v_exp_f32_e32 v90, v84
	v_exp_f32_e32 v91, v85
	v_lshlrev_b32_e32 v92, 16, v106
	v_and_b32_e32 v93, s89, v106
	v_mul_f32_e32 v92, v92, v90
	v_mul_f32_e32 v93, v93, v91
	ds_write_b64 v83, v[92:93] offset:8192
	ds_write_b64 v83, v[86:87] offset:16384
	v_lshlrev_b32_e32 v94, 16, v110
	v_and_b32_e32 v95, s89, v110
	v_mul_f32_e32 v94, v94, v90
	v_mul_f32_e32 v95, v95, v91
	ds_write_b64 v83, v[94:95] offset:24576
	v_lshlrev_b32_e32 v92, 16, v114
	v_and_b32_e32 v93, s89, v114
	v_mul_f32_e32 v92, v92, v86
	v_mul_f32_e32 v93, v93, v87
	ds_write_b64 v83, v[92:93] offset:32768
	v_lshlrev_b32_e32 v92, 16, v99
	v_and_b32_e32 v93, s89, v99
	v_fmac_f32_e32 v84, 0x3fb8aa3b, v92
	v_fmac_f32_e32 v85, 0x3fb8aa3b, v93
	v_lshlrev_b32_e32 v94, 16, v103
	v_and_b32_e32 v95, s89, v103
	v_mul_f32_e32 v94, v94, v86
	v_mul_f32_e32 v95, v95, v87
	ds_write_b64 v83, v[94:95] offset:256
	v_exp_f32_e64 v88, -v84
	v_exp_f32_e64 v89, -v85
	v_exp_f32_e32 v90, v84
	v_exp_f32_e32 v91, v85
	v_lshlrev_b32_e32 v92, 16, v107
	v_and_b32_e32 v93, s89, v107
	v_mul_f32_e32 v92, v92, v90
	v_mul_f32_e32 v93, v93, v91
	ds_write_b64 v83, v[92:93] offset:8448
	ds_write_b64 v83, v[88:89] offset:16640
	v_lshlrev_b32_e32 v94, 16, v111
	v_and_b32_e32 v95, s89, v111
	v_mul_f32_e32 v94, v94, v90
	v_mul_f32_e32 v95, v95, v91
	ds_write_b64 v83, v[94:95] offset:24832
	v_lshlrev_b32_e32 v92, 16, v115
	v_and_b32_e32 v93, s89, v115
	v_mul_f32_e32 v92, v92, v88
	v_mul_f32_e32 v93, v93, v89
	ds_write_b64 v83, v[92:93] offset:33024
	v_lshlrev_b32_e32 v92, 16, v100
	v_and_b32_e32 v93, s89, v100
	v_fmac_f32_e32 v84, 0x3fb8aa3b, v92
	v_fmac_f32_e32 v85, 0x3fb8aa3b, v93
	v_lshlrev_b32_e32 v94, 16, v104
	v_and_b32_e32 v95, s89, v104
	v_mul_f32_e32 v94, v94, v88
	v_mul_f32_e32 v95, v95, v89
	ds_write_b64 v83, v[94:95] offset:512
	v_exp_f32_e64 v86, -v84
	v_exp_f32_e64 v87, -v85
	v_exp_f32_e32 v90, v84
	v_exp_f32_e32 v91, v85
	v_lshlrev_b32_e32 v92, 16, v108
	v_and_b32_e32 v93, s89, v108
	v_mul_f32_e32 v92, v92, v90
	v_mul_f32_e32 v93, v93, v91
	ds_write_b64 v83, v[92:93] offset:8704
	ds_write_b64 v83, v[86:87] offset:16896
	v_lshlrev_b32_e32 v94, 16, v112
	v_and_b32_e32 v95, s89, v112
	v_mul_f32_e32 v94, v94, v90
	v_mul_f32_e32 v95, v95, v91
	ds_write_b64 v83, v[94:95] offset:25088
	v_lshlrev_b32_e32 v92, 16, v116
	v_and_b32_e32 v93, s89, v116
	v_mul_f32_e32 v92, v92, v86
	v_mul_f32_e32 v93, v93, v87
	ds_write_b64 v83, v[92:93] offset:33280
	v_lshlrev_b32_e32 v92, 16, v101
	v_and_b32_e32 v93, s89, v101
	v_fmac_f32_e32 v84, 0x3fb8aa3b, v92
	v_fmac_f32_e32 v85, 0x3fb8aa3b, v93
	v_lshlrev_b32_e32 v94, 16, v105
	v_and_b32_e32 v95, s89, v105
	v_mul_f32_e32 v94, v94, v86
	v_mul_f32_e32 v95, v95, v87
	ds_write_b64 v83, v[94:95] offset:768
	v_exp_f32_e64 v88, -v84
	v_exp_f32_e64 v89, -v85
	v_exp_f32_e32 v90, v84
	v_exp_f32_e32 v91, v85
	v_lshlrev_b32_e32 v92, 16, v109
	v_and_b32_e32 v93, s89, v109
	v_mul_f32_e32 v92, v92, v90
	v_mul_f32_e32 v93, v93, v91
	ds_write_b64 v83, v[92:93] offset:8960
	ds_write_b64 v83, v[88:89] offset:17152
	v_lshlrev_b32_e32 v94, 16, v113
	v_and_b32_e32 v95, s89, v113
	v_mul_f32_e32 v94, v94, v90
	v_mul_f32_e32 v95, v95, v91
	ds_write_b64 v83, v[94:95] offset:25344
	v_lshlrev_b32_e32 v92, 16, v117
	v_and_b32_e32 v93, s89, v117
	ds_write_b64 v83, v[92:93] offset:33536
